# speedup vs baseline: 1.1095x; 1.0056x over previous
.LBB3_20:
	s_or_b64 exec, exec, s[6:7]
	s_load_dwordx2 s[12:13], s[0:1], 0x30
	v_min_u32_e32 v47, 27, v50
	v_min_u32_e32 v2, 3, v48
	v_or_b32_e32 v56, 24, v2
	v_lshrrev_b32_e32 v122, 4, v1
	v_and_b32_e32 v93, 15, v0
	v_lshrrev_b32_e32 v120, 8, v0
	s_lshl_b32 s18, s24, 18
	v_and_b32_e32 v121, 3, v48
	v_lshl_or_b32 v123, v120, 4, v93
	s_movk_i32 s0, 0x42
	s_cmp_lg_u32 0, -1
	v_mad_u32_u24 v1, v121, s0, v123
	s_cselect_b32 s0, 0, 0
	v_lshlrev_b32_e32 v2, 7, v1
	v_bitop3_b32 v3, v1, v122, 7 bitop3:0x6c
	v_add_u32_e32 v1, 33, v1
	s_add_i32 s1, s0, 0xc600
	v_lshl_or_b32 v126, v3, 4, v2
	v_lshlrev_b32_e32 v2, 7, v1
	v_bitop3_b32 v1, v1, v122, 7 bitop3:0x6c
	v_add_u32_e32 v124, s1, v46
	s_add_i32 s1, s0, 0xca00
	v_lshl_or_b32 v127, v1, 4, v2
	v_add_u32_e32 v1, s1, v46
	s_add_i32 s1, s0, 0xce00
	s_waitcnt vmcnt(0)
	s_waitcnt lgkmcnt(0)
	s_barrier
	ds_read_b128 v[42:45], v124
	ds_read_b128 v[38:41], v1
	v_add_u32_e32 v1, s1, v46
	s_add_i32 s1, s0, 0xd200
	ds_read_b128 v[34:37], v1
	v_add_u32_e32 v1, s1, v46
	s_add_i32 s1, s0, 0xd600
	ds_read_b128 v[30:33], v1
	v_add_u32_e32 v1, s1, v46
	s_add_i32 s1, s0, 0xda00
	ds_read_b128 v[26:29], v1
	v_add_u32_e32 v1, s1, v46
	s_add_i32 s1, s0, 0xde00
	ds_read_b128 v[22:25], v1
	v_add_u32_e32 v1, s1, v46
	s_add_i32 s1, s0, 0xe200
	ds_read_b128 v[10:13], v1
	v_add_u32_e32 v1, s1, v46
	s_add_i32 s1, s0, 0xe600
	ds_read_b128 v[6:9], v1
	v_add_u32_e32 v1, s1, v46
	ds_read_b128 v[2:5], v1
	v_add_u32_e32 v1, s0, v126
	ds_read_b128 v[14:17], v1
	v_add_u32_e32 v1, s0, v127
	s_add_i32 s0, s0, 0xea00
	v_add_u32_e32 v125, s0, v46
	s_lshl_b32 s0, s24, 20
	s_add_u32 s10, s2, s0
	v_mov_b32_e32 v95, 0
	v_lshlrev_b32_e32 v0, 4, v0
	ds_read_b128 v[18:21], v1
	s_addc_u32 s11, s3, 0
	v_lshlrev_b32_e32 v91, 10, v47
	v_and_b32_e32 v0, 0x1c00, v0
	v_mov_b32_e32 v1, v95
	v_mov_b32_e32 v47, 0x28800
	s_add_u32 s0, s10, 0x400000
	v_mad_u64_u32 v[54:55], s[2:3], s24, v47, v[0:1]
	s_addc_u32 s1, s11, 0
	v_lshlrev_b32_e32 v48, 2, v94
	v_mov_b32_e32 v49, v95
	v_lshlrev_b32_e32 v50, 2, v96
	v_mov_b32_e32 v51, v95
	v_lshlrev_b32_e32 v52, 2, v98
	v_mov_b32_e32 v53, v95
	v_or_b32_e32 v54, v54, v46
	v_lshlrev_b32_e32 v46, 2, v100
	v_mov_b32_e32 v47, v95
	s_waitcnt lgkmcnt(0)
	v_lshl_add_u64 v[0:1], s[0:1], 0, v[48:49]
	v_lshl_add_u64 v[106:107], s[0:1], 0, v[50:51]
	v_lshl_add_u64 v[110:111], s[0:1], 0, v[52:53]
	v_lshl_add_u64 v[112:113], s[10:11], 0, v[46:47]
	v_lshl_add_u64 v[114:115], s[0:1], 0, v[46:47]
	v_lshl_add_u64 v[46:47], s[20:21], 0, v[54:55]
	s_mov_b64 s[0:1], 0xd000
	v_lshl_add_u64 v[116:117], v[46:47], 0, s[0:1]
	s_movk_i32 s0, 0xc000
	s_movk_i32 s2, 0xe000
	s_mov_b32 s19, 0
	v_lshl_add_u64 v[102:103], s[10:11], 0, v[48:49]
	v_mov_b32_e32 v97, v95
	v_mov_b32_e32 v99, v95
	v_mov_b32_e32 v101, v95
	v_lshlrev_b32_e32 v119, 10, v56
	v_lshl_add_u64 v[104:105], s[10:11], 0, v[50:51]
	v_lshl_add_u64 v[108:109], s[10:11], 0, v[52:53]
	s_mov_b32 s20, 1
	s_mov_b32 s1, -1
	s_mov_b32 s3, -1
	s_add_i32 s17, 0, 0x16000
	s_add_i32 s16, 0, 0x1d000
	s_mov_b64 s[6:7], 0x4800
	v_readfirstlane_b32 s32, v118
	v_readfirstlane_b32 s33, v90
	v_readfirstlane_b32 s34, v92
	s_nop 3
	s_add_i32 s32, s32, 0xc600
	s_add_i32 s33, s33, 0xc600
	s_add_i32 s34, s34, 0xc600
	s_cmp_ge_u32 s32, 0xd600
	s_cbranch_scc0 .Lk3_noprio
	s_setprio 1
.Lk3_noprio:
.Lk3_top:
	s_bitcmp1_b32 s19, 0
	s_cselect_b32 s14, 0x4800, 0
	v_add_u32_e32 v78, s14, v125
	s_waitcnt lgkmcnt(8)
	v_mfma_f32_16x16x32_f16 a[0:3], v[42:45], v[14:17], a[0:3]
	ds_read_b128 v[70:73], v78
	s_add_i32 s15, s19, 1
	v_mfma_f32_16x16x32_f16 a[4:7], v[42:45], v[18:21], a[4:7]
	ds_read_b128 v[66:69], v78 offset:1024
	s_mul_hi_u32 s28, s15, 0xaaaaaaab
	s_waitcnt lgkmcnt(9)
	v_mfma_f32_16x16x32_f16 a[12:15], v[38:41], v[14:17], a[12:15]
	ds_read_b128 v[58:61], v78 offset:2048
	s_lshr_b32 s28, s28, 1
	s_bitcmp1_b32 s15, 0
	s_cselect_b32 s31, 0x4800, 0
	v_mfma_f32_16x16x32_f16 a[16:19], v[38:41], v[18:21], a[16:19]
	ds_read_b128 v[54:57], v78 offset:3072
	s_mul_i32 s29, s28, 3
	v_xor_b32_e32 v82, 64, v126
	s_waitcnt lgkmcnt(10)
	v_mfma_f32_16x16x32_f16 a[28:31], v[34:37], v[14:17], a[28:31]
	ds_read_b128 v[46:49], v78 offset:4096
	s_sub_i32 s29, s15, s29
	v_xor_b32_e32 v86, 64, v127
	v_mfma_f32_16x16x32_f16 a[60:63], v[34:37], v[18:21], a[60:63]
	ds_read_b128 v[50:53], v78 offset:5120
	s_add_i32 s30, s29, 1
	v_add_lshl_u32 v128, s28, v121, 1
	s_waitcnt lgkmcnt(11)
	v_mfma_f32_16x16x32_f16 a[8:11], v[30:33], v[14:17], a[8:11]
	ds_read_b128 v[62:65], v78 offset:6144
	v_and_or_b32 v129, s29, 1, v128
	v_mfma_f32_16x16x32_f16 a[20:23], v[30:33], v[18:21], a[20:23]
	ds_read_b128 v[74:77], v78 offset:7168
	v_and_or_b32 v130, s30, 1, v128
	s_lshr_b32 s29, s29, 1
	s_lshr_b32 s30, s30, 1
	s_waitcnt lgkmcnt(12)
	v_mfma_f32_16x16x32_f16 a[24:27], v[26:29], v[14:17], a[24:27]
	ds_read_b128 v[78:81], v78 offset:8192
	v_lshl_add_u32 v129, v129, 5, v129
	v_mfma_f32_16x16x32_f16 a[36:39], v[26:29], v[18:21], a[36:39]
	ds_read_b128 v[82:85], v82
	v_lshl_add_u32 v130, v130, 5, v130
	s_waitcnt lgkmcnt(13)
	v_mfma_f32_16x16x32_f16 a[44:47], v[22:25], v[14:17], a[44:47]
	ds_read_b128 v[86:89], v86
	v_add3_u32 v129, v123, s29, v129
	v_mfma_f32_16x16x32_f16 a[64:67], v[22:25], v[18:21], a[64:67]
	v_add3_u32 v130, v123, s30, v130
	v_lshlrev_b32_e32 v128, 7, v129
	s_waitcnt lgkmcnt(13)
	v_mfma_f32_16x16x32_f16 a[32:35], v[10:13], v[14:17], a[32:35]
	v_bitop3_b32 v129, v129, v122, 7 bitop3:0x6c
	v_lshlrev_b32_e32 v136, 7, v130
	v_mfma_f32_16x16x32_f16 a[40:43], v[10:13], v[18:21], a[40:43]
	v_bitop3_b32 v130, v130, v122, 7 bitop3:0x6c
	v_lshl_or_b32 v126, v129, 4, v128
	s_waitcnt lgkmcnt(12)
	v_mfma_f32_16x16x32_f16 a[48:51], v[6:9], v[14:17], a[48:51]
	v_lshl_or_b32 v127, v130, 4, v136
	v_add_u32_e32 v131, s31, v124
	v_mfma_f32_16x16x32_f16 a[52:55], v[6:9], v[18:21], a[52:55]
	v_lshl_add_u64 v[132:133], v[116:117], 0, s[0:1]
	s_add_i32 s35, s32, s14
	s_waitcnt lgkmcnt(11)
	v_mfma_f32_16x16x32_f16 a[56:59], v[2:5], v[14:17], a[56:59]
	v_lshl_add_u64 v[134:135], v[116:117], 0, s[2:3]
	s_add_i32 s36, s33, s14
	s_add_i32 s37, s34, s14
	v_mfma_f32_16x16x32_f16 a[68:71], v[2:5], v[18:21], a[68:71]
	s_cmp_eq_u32 s19, 8
	s_waitcnt lgkmcnt(0)
	s_cbranch_scc1 .Lk3_nb
	s_waitcnt vmcnt(0)

.LBB3_32:
	s_setprio 0
	v_lshl_add_u32 v0, v120, 5, s22
	v_or_b32_e32 v1, s23, v121
	s_movk_i32 s0, 0x7f
	v_lshl_or_b32 v7, v93, 1, v0
	s_movk_i32 s1, 0x7e
	s_nop 15
	s_nop 15
	v_cmp_eq_u32_e64 s[4:5], s1, v7
	s_nop 7
	v_cmp_gt_u32_e32 vcc, s0, v1
	v_accvgpr_read_b32 v5, a14
	v_cmp_eq_u32_e64 s[0:1], 0, v1
	v_or_b32_e32 v4, v93, v7
	v_cmp_eq_u32_e64 s[2:3], 0, v4
	v_cndmask_b32_e64 v14, v5, 0, s[0:1]
	v_accvgpr_read_b32 v5, a13
	v_cndmask_b32_e64 v22, v5, 0, s[0:1]
	v_accvgpr_read_b32 v5, a12
	v_cndmask_b32_e64 v116, v5, 0, s[0:1]
	v_accvgpr_read_b32 v5, a49
	v_cndmask_b32_e32 v16, 0, v5, vcc
	v_accvgpr_read_b32 v5, a48
	v_cndmask_b32_e32 v28, 0, v5, vcc
	v_accvgpr_read_b32 v5, a30
	v_cndmask_b32_e64 v10, v5, 0, s[0:1]
	v_accvgpr_read_b32 v5, a29
	v_cndmask_b32_e64 v24, v5, 0, s[0:1]
	v_accvgpr_read_b32 v5, a28
	v_cndmask_b32_e64 v42, v5, 0, s[0:1]
	v_accvgpr_read_b32 v5, a57
	v_cndmask_b32_e32 v20, 0, v5, vcc
	v_accvgpr_read_b32 v5, a56
	v_cndmask_b32_e32 v38, 0, v5, vcc
	v_accvgpr_read_b32 v5, a6
	v_cndmask_b32_e64 v15, v5, 0, s[0:1]
	v_accvgpr_read_b32 v5, a5
	v_cndmask_b32_e64 v23, v5, 0, s[0:1]
	v_accvgpr_read_b32 v5, a4
	v_cndmask_b32_e64 v117, v5, 0, s[0:1]
	v_accvgpr_read_b32 v5, a41
	v_cndmask_b32_e32 v17, 0, v5, vcc
	v_accvgpr_read_b32 v5, a40
	v_cndmask_b32_e32 v29, 0, v5, vcc
	v_accvgpr_read_b32 v5, a17
	v_cndmask_b32_e64 v37, v5, 0, s[0:1]
	v_accvgpr_read_b32 v5, a16
	v_cndmask_b32_e64 v47, v5, 0, s[0:1]
	v_accvgpr_read_b32 v5, a52
	v_cndmask_b32_e32 v45, 0, v5, vcc
	v_accvgpr_read_b32 v5, a68
	v_cndmask_b32_e32 v12, 0, v5, vcc
	v_accvgpr_read_b32 v5, a0
	s_or_b64 s[8:9], s[2:3], s[0:1]
	v_cmp_eq_u32_e64 s[6:7], 15, v93
	v_accvgpr_read_b32 v11, a8
	v_cndmask_b32_e64 v112, v5, 0, s[8:9]
	v_accvgpr_read_b32 v4, a67
	v_mov_b32_e32 v5, 0x90
	s_and_b64 s[4:5], s[6:7], s[4:5]
	v_mov_b64_e32 v[40:41], v[16:17]
	v_cndmask_b32_e64 v16, v11, 0, s[2:3]
	v_cndmask_b32_e64 v11, 12, v5, s[6:7]
	v_cndmask_b32_e64 v61, v4, 0, s[4:5]
	v_accvgpr_read_b32 v4, a61
	s_or_b64 s[6:7], s[4:5], s[0:1]
	v_cndmask_b32_e64 v87, v4, 0, s[6:7]
	v_accvgpr_read_b32 v4, a60
	v_cndmask_b32_e64 v86, v4, 0, s[6:7]
	v_accvgpr_read_b32 v4, a65
	v_cndmask_b32_e64 v5, v4, 0, s[4:5]
	v_accvgpr_read_b32 v4, a64
	v_cndmask_b32_e64 v4, v4, 0, s[4:5]
	s_lshl_b32 s14, s18, 2
	v_mov_b64_e32 v[32:33], v[4:5]
	v_lshl_or_b32 v4, v122, 18, s14
	v_mov_b32_e32 v5, 0
	v_mov_b64_e32 v[62:63], v[14:15]
	v_lshl_add_u64 v[14:15], s[12:13], 0, v[4:5]
	v_lshlrev_b32_e32 v4, 7, v1
	v_lshl_add_u64 v[14:15], v[4:5], 2, v[14:15]
	v_lshlrev_b32_e32 v4, 2, v7
	v_mul_u32_u24_e32 v1, 24, v122
	v_lshl_add_u64 v[54:55], v[14:15], 0, v[4:5]
	v_mbcnt_lo_u32_b32 v138, -1, 0
	v_mbcnt_hi_u32_b32 v138, -1, v138
	v_and_b32_e32 v138, 1, v138
	v_mul_u32_u24_e32 v138, 0xfff8, v138
	v_add_u32_e32 v138, 0xffff0000, v138
	v_mov_b32_e32 v139, -1
	v_lshl_add_u64 v[134:135], v[54:55], 0, v[138:139]
	s_mov_b32 s28, 0x55555555
	s_mov_b32 s29, 0x55555555
	s_mov_b32 s30, 0xaaaaaaaa
	s_mov_b32 s31, 0xaaaaaaaa
	v_or_b32_e32 v1, v1, v121
	v_lshlrev_b32_e32 v4, 7, v120
	s_movk_i32 s12, 0x120
	v_mad_u32_u24 v1, v1, s12, v4
	s_add_u32 s12, s10, 0x800000
	v_accvgpr_read_b32 v7, a72
	v_mov_b64_e32 v[80:81], v[28:29]
	s_addc_u32 s13, s11, 0
	v_lshlrev_b64 v[28:29], 2, v[94:95]
	v_readfirstlane_b32 s14, v7
	v_add_u32_e32 v7, 0, v90
	v_lshl_add_u64 v[4:5], s[12:13], 0, v[28:29]
	s_mov_b32 m0, s14
	v_lshlrev_b64 v[30:31], 2, v[96:97]
	v_readfirstlane_b32 s14, v7
	v_mov_b32_e32 v14, v7
	v_add_u32_e32 v7, 0, v91
	s_waitcnt lgkmcnt(0)
	s_barrier
	global_load_lds_dwordx4 v[4:5], off nt
	v_lshl_add_u64 v[4:5], s[12:13], 0, v[30:31]
	s_mov_b32 m0, s14
	v_lshlrev_b64 v[56:57], 2, v[98:99]
	v_readfirstlane_b32 s14, v7
	global_load_lds_dwordx4 v[4:5], off nt
	v_lshl_add_u64 v[4:5], s[12:13], 0, v[56:57]
	v_mov_b32_e32 v19, v7
	s_mov_b32 m0, s14
	v_lshlrev_b64 v[58:59], 2, v[100:101]
	v_add_u32_e32 v7, 0, v119
	v_accvgpr_read_b32 v25, a72
	global_load_lds_dwordx4 v[4:5], off nt
	v_lshl_add_u64 v[4:5], s[12:13], 0, v[58:59]
	v_readfirstlane_b32 s12, v7
	v_mov_b32_e32 v21, v7
	s_mov_b32 m0, s12
	s_add_u32 s12, s10, 0xc00000
	v_add_u32_e32 v7, 0x7000, v25
	s_addc_u32 s13, s11, 0
	v_readfirstlane_b32 s14, v7
	v_add_u32_e32 v7, 0x7000, v14
	global_load_lds_dwordx4 v[4:5], off nt
	v_lshl_add_u64 v[4:5], s[12:13], 0, v[28:29]
	s_mov_b32 m0, s14
	v_readfirstlane_b32 s14, v7
	v_add_u32_e32 v7, 0x7000, v19
	global_load_lds_dwordx4 v[4:5], off nt
	v_lshl_add_u64 v[4:5], s[12:13], 0, v[30:31]
	s_mov_b32 m0, s14
	v_readfirstlane_b32 s14, v7
	global_load_lds_dwordx4 v[4:5], off nt
	v_lshl_add_u64 v[4:5], s[12:13], 0, v[56:57]
	s_mov_b32 m0, s14
	v_add_u32_e32 v7, 0x7000, v21
	global_load_lds_dwordx4 v[4:5], off nt
	v_lshl_add_u64 v[4:5], s[12:13], 0, v[58:59]
	v_readfirstlane_b32 s12, v7
	s_mov_b32 m0, s12
	s_add_u32 s12, s10, 0x1000000
	v_add_u32_e32 v7, 0xe000, v25
	s_addc_u32 s13, s11, 0
	v_readfirstlane_b32 s14, v7
	v_add_u32_e32 v7, 0xe000, v14
	global_load_lds_dwordx4 v[4:5], off nt
	v_lshl_add_u64 v[4:5], s[12:13], 0, v[28:29]
	s_mov_b32 m0, s14
	v_readfirstlane_b32 s14, v7
	v_add_u32_e32 v7, 0xe000, v19
	global_load_lds_dwordx4 v[4:5], off nt
	v_lshl_add_u64 v[4:5], s[12:13], 0, v[30:31]
	s_mov_b32 m0, s14
	v_readfirstlane_b32 s14, v7
	global_load_lds_dwordx4 v[4:5], off nt
	v_lshl_add_u64 v[4:5], s[12:13], 0, v[56:57]
	s_mov_b32 m0, s14
	v_add_u32_e32 v7, 0xe000, v21
	global_load_lds_dwordx4 v[4:5], off nt
	v_lshl_add_u64 v[4:5], s[12:13], 0, v[58:59]
	v_readfirstlane_b32 s12, v7
	s_mov_b32 m0, s12
	v_lshl_add_u32 v15, v93, 3, v1
	global_load_lds_dwordx4 v[4:5], off nt
	v_add_u32_e32 v1, v1, v11
	s_waitcnt vmcnt(16)
	v_accvgpr_write_b32 a12, v14
	v_mov_b64_e32 v[124:125], v[56:57]
	v_accvgpr_write_b32 a13, v19
	v_mov_b64_e32 v[126:127], v[58:59]
	v_accvgpr_write_b32 a16, v21
	s_waitcnt lgkmcnt(0)
	s_barrier
	v_add_u32_e32 v14, 0x16010, v15
	v_mov_b32_e32 v122, v15
	v_add_u32_e32 v15, 0x16000, v1
	ds_read_b64 v[64:65], v14
	ds_read_b64 v[66:67], v14 offset:288
	ds_read_b64 v[68:69], v14 offset:576
	ds_read_b64 v[76:77], v14 offset:1728
	ds_read_b64 v[78:79], v14 offset:2016
	ds_read_b64 v[4:5], v14 offset:2304
	ds_read_b64 v[84:85], v14 offset:3456
	ds_read_b64 v[74:75], v14 offset:3744
	ds_read_b64 v[88:89], v14 offset:4032
	ds_read_b64 v[100:101], v14 offset:5184
	ds_read_b64 v[106:107], v14 offset:5472
	ds_read_b64 v[120:121], v14 offset:5760
	ds_read_b32 v43, v15
	ds_read_b32 v19, v15 offset:288
	ds_read_b32 v39, v15 offset:576
	ds_read_b32 v25, v15 offset:1728
	ds_read_b32 v7, v15 offset:2016
	ds_read_b32 v21, v15 offset:2304
	ds_read_b32 v11, v15 offset:3456
	ds_read_b32 v35, v15 offset:3744
	ds_read_b32 v59, v15 offset:4032
	ds_read_b32 v57, v15 offset:5184
	ds_read_b32 v51, v15 offset:5472
	ds_read_b32 v49, v15 offset:5760
	s_waitcnt lgkmcnt(0)
	v_accvgpr_read_b32 v8, a26
	v_mov_b32_e32 v46, v43
	v_mov_b32_e32 v113, v65
	v_mov_b32_e32 v26, v19
	v_mov_b32_dpp v46, v65 row_shr:1 row_mask:0xf bank_mask:0xf
	v_pk_mul_f32 v[70:71], v[112:113], v[46:47]
	v_accvgpr_read_b32 v9, a22
	v_accvgpr_read_b32 v27, a36
	v_mov_b32_dpp v43, v64 row_shl:1 row_mask:0xf bank_mask:0xf
	v_mov_b32_dpp v26, v67 row_shr:1 row_mask:0xf bank_mask:0xf
	v_pk_fma_f32 v[70:71], v[64:65], v[116:117], v[70:71] op_sel_hi:[0,1,1]
	v_pk_mov_b32 v[64:65], v[64:65], v[86:87] op_sel:[1,0]
	v_mov_b32_e32 v17, v67
	v_mov_b64_e32 v[102:103], v[8:9]
	v_accvgpr_read_b32 v8, a25
	v_accvgpr_read_b32 v114, a24
	v_accvgpr_read_b32 v9, a21
	v_accvgpr_read_b32 v115, a20
	v_accvgpr_read_b32 v2, a32
	v_mov_b64_e32 v[82:83], v[30:31]
	v_pk_fma_f32 v[70:71], v[64:65], v[42:43], v[70:71]
	v_pk_mul_f32 v[64:65], v[16:17], v[26:27]
	v_mov_b64_e32 v[30:31], v[32:33]
	v_accvgpr_read_b32 v18, a44
	v_mov_b64_e32 v[104:105], v[8:9]
	v_cndmask_b32_e32 v9, 0, v2, vcc
	v_accvgpr_write_b32 a4, v14
	v_mov_b32_dpp v19, v66 row_shl:1 row_mask:0xf bank_mask:0xf
	v_pk_fma_f32 v[64:65], v[66:67], v[114:115], v[64:65] op_sel_hi:[0,1,1]
	v_pk_mov_b32 v[66:67], v[66:67], v[30:31] op_sel:[1,0]
	v_accvgpr_read_b32 v14, a69
	v_mov_b32_e32 v44, v39
	v_mov_b32_e32 v60, v1
	v_pk_fma_f32 v[66:67], v[66:67], v[18:19], v[64:65]
	v_cndmask_b32_e32 v14, 0, v14, vcc
	v_cndmask_b32_e64 v0, v9, 0, s[2:3]
	v_mov_b32_dpp v44, v69 row_shr:1 row_mask:0xf bank_mask:0xf
	v_pk_add_f32 v[70:71], v[70:71], 0 op_sel_hi:[1,0]
	v_mov_b32_e32 v1, v69
	v_accvgpr_write_b32 a0, v15
	v_cndmask_b32_e64 v15, v14, 0, s[4:5]
	v_cndmask_b32_e64 v14, v12, 0, s[4:5]
	v_pk_add_f32 v[66:67], v[70:71], v[66:67]
	v_pk_mul_f32 v[70:71], v[0:1], v[44:45]
	v_mov_b32_dpp v39, v68 row_shl:1 row_mask:0xf bank_mask:0xf
	v_pk_fma_f32 v[70:71], v[68:69], v[80:81], v[70:71] op_sel_hi:[0,1,1]
	v_pk_mov_b32 v[68:69], v[68:69], v[14:15] op_sel:[1,0]
	v_accvgpr_read_b32 v9, a1
	v_pk_fma_f32 v[68:69], v[68:69], v[38:39], v[70:71]
	v_mov_b32_e32 v36, v25
	v_cndmask_b32_e64 v64, v9, 0, s[8:9]
	v_pk_add_f32 v[66:67], v[66:67], v[68:69]
	v_mov_b32_dpp v36, v77 row_shr:1 row_mask:0xf bank_mask:0xf
	v_mov_b32_e32 v65, v77
	v_mov_b64_e32 v[108:109], v[22:23]
	v_accvgpr_read_b32 v9, a9
	v_mov_b32_e32 v128, v66
	v_mov_b32_e32 v129, v67
	v_mov_b32_e32 v12, v7
	v_pk_mul_f32 v[66:67], v[64:65], v[36:37]
	v_accvgpr_read_b32 v13, a37
	v_mov_b64_e32 v[72:73], v[28:29]
	v_cndmask_b32_e64 v28, v9, 0, s[2:3]
	v_mov_b32_dpp v25, v76 row_shl:1 row_mask:0xf bank_mask:0xf
	v_mov_b32_dpp v12, v79 row_shr:1 row_mask:0xf bank_mask:0xf
	v_pk_fma_f32 v[66:67], v[76:77], v[108:109], v[66:67] op_sel_hi:[0,1,1]
	v_mov_b32_e32 v76, v77
	v_mov_b32_e32 v77, v87
	v_mov_b32_e32 v29, v79
	v_pk_fma_f32 v[66:67], v[76:77], v[24:25], v[66:67]
	v_pk_mul_f32 v[76:77], v[28:29], v[12:13]
	v_accvgpr_read_b32 v6, a45
	v_accvgpr_read_b32 v2, a33
	v_mov_b32_dpp v7, v78 row_shl:1 row_mask:0xf bank_mask:0xf
	v_pk_fma_f32 v[76:77], v[78:79], v[104:105], v[76:77] op_sel_hi:[0,1,1]
	v_mov_b32_e32 v78, v79
	v_mov_b32_e32 v79, v31
	v_cndmask_b32_e32 v2, 0, v2, vcc
	v_accvgpr_read_b32 v50, a53
	v_pk_fma_f32 v[76:77], v[78:79], v[6:7], v[76:77]
	v_mov_b32_e32 v78, v21
	v_accvgpr_write_b32 a44, v80
	v_cndmask_b32_e32 v79, 0, v50, vcc
	v_cndmask_b32_e64 v52, v2, 0, s[2:3]
	v_mov_b32_dpp v78, v5 row_shr:1 row_mask:0xf bank_mask:0xf
	v_pk_add_f32 v[66:67], v[66:67], 0 op_sel_hi:[1,0]
	v_mov_b32_e32 v53, v5
	v_accvgpr_write_b32 a45, v81
	v_accvgpr_write_b32 a21, v15
	v_pk_add_f32 v[80:81], v[66:67], v[76:77]
	v_pk_mul_f32 v[66:67], v[52:53], v[78:79]
	v_accvgpr_write_b32 a24, v40
	v_accvgpr_read_b32 v2, a2
	v_mov_b32_dpp v21, v4 row_shl:1 row_mask:0xf bank_mask:0xf
	v_pk_fma_f32 v[66:67], v[4:5], v[40:41], v[66:67] op_sel_hi:[0,1,1]
	v_accvgpr_write_b32 a25, v41
	v_mov_b32_e32 v4, v5
	v_accvgpr_read_b32 v5, a21
	v_cndmask_b32_e64 v40, v2, 0, s[8:9]
	v_accvgpr_read_b32 v2, a62
	v_accvgpr_read_b32 v8, a18
	v_accvgpr_read_b32 v48, a63
	v_accvgpr_write_b32 a20, v14
	v_accvgpr_write_b32 a41, v23
	v_pk_fma_f32 v[4:5], v[4:5], v[20:21], v[66:67]
	s_mov_b64 s[12:13], 0x10000
	v_cndmask_b32_e64 v14, v2, 0, s[6:7]
	v_mov_b32_e32 v76, v11
	v_accvgpr_read_b32 v2, a10
	v_accvgpr_write_b32 a40, v22
	v_cndmask_b32_e64 v15, v48, 0, s[6:7]
	v_cndmask_b32_e64 v77, v8, 0, s[0:1]
	v_pk_add_f32 v[4:5], v[80:81], v[4:5]
	v_lshl_add_u64 v[136:137], v[134:135], 0, s[12:13]
	v_mov_b32_dpp v76, v85 row_shr:1 row_mask:0xf bank_mask:0xf
	v_mov_b32_e32 v41, v85
	v_cndmask_b32_e64 v22, v2, 0, s[2:3]
	v_mov_b32_e32 v2, v35
	v_accvgpr_read_b32 v1, a50
	v_accvgpr_read_b32 v3, a38
	s_mov_b64 s[32:33], vcc
	s_nop 1
	s_mov_b64 vcc, s[28:29]
	s_nop 0
	v_cndmask_b32_dpp v130, v4, v128, vcc quad_perm:[1,0,3,2] row_mask:0xf bank_mask:0xf
	v_cndmask_b32_dpp v131, v5, v129, vcc quad_perm:[1,0,3,2] row_mask:0xf bank_mask:0xf
	s_mov_b64 vcc, s[30:31]
	s_nop 0
	v_cndmask_b32_dpp v132, v128, v4, vcc quad_perm:[1,0,3,2] row_mask:0xf bank_mask:0xf
	v_cndmask_b32_dpp v133, v129, v5, vcc quad_perm:[1,0,3,2] row_mask:0xf bank_mask:0xf
	global_store_dwordx4 v[136:137], v[130:133], off sc0 sc1 nt
	s_nop 1
	s_mov_b64 vcc, s[32:33]
	v_mov_b64_e32 v[8:9], v[14:15]
	v_pk_mul_f32 v[4:5], v[40:41], v[76:77]
	v_mov_b64_e32 v[66:67], v[62:63]
	v_mov_b32_dpp v2, v75 row_shr:1 row_mask:0xf bank_mask:0xf
	v_mov_b32_e32 v23, v75
	v_cndmask_b32_e32 v62, 0, v1, vcc
	v_accvgpr_read_b32 v1, a42
	v_mov_b32_dpp v11, v84 row_shl:1 row_mask:0xf bank_mask:0xf
	v_pk_fma_f32 v[4:5], v[84:85], v[66:67], v[4:5] op_sel_hi:[0,1,1]
	v_pk_mov_b32 v[80:81], v[84:85], v[8:9] op_sel:[1,0]
	v_pk_mul_f32 v[84:85], v[22:23], v[2:3]
	v_accvgpr_read_b32 v2, a58
	v_cndmask_b32_e32 v63, 0, v1, vcc
	v_accvgpr_read_b32 v1, a70
	v_pk_fma_f32 v[80:81], v[80:81], v[10:11], v[4:5]
	v_accvgpr_read_b32 v4, a66
	v_cndmask_b32_e32 v58, 0, v2, vcc
	v_cndmask_b32_e32 v1, 0, v1, vcc
	v_accvgpr_read_b32 v2, a71
	v_cndmask_b32_e64 v8, v4, 0, s[4:5]
	v_cndmask_b32_e32 v2, 0, v2, vcc
	v_cndmask_b32_e64 v4, v1, 0, s[4:5]
	v_accvgpr_read_b32 v1, a34
	v_mov_b32_e32 v9, v61
	v_cndmask_b32_e64 v5, v2, 0, s[4:5]
	v_cndmask_b32_e32 v1, 0, v1, vcc
	v_accvgpr_read_b32 v2, a54
	v_mov_b32_e32 v92, v59
	v_accvgpr_read_b32 v34, a46
	v_mov_b32_dpp v35, v74 row_shl:1 row_mask:0xf bank_mask:0xf
	v_pk_fma_f32 v[84:85], v[74:75], v[102:103], v[84:85] op_sel_hi:[0,1,1]
	v_pk_mov_b32 v[74:75], v[74:75], v[8:9] op_sel:[1,0]
	v_cndmask_b32_e32 v93, 0, v2, vcc
	v_mov_b32_dpp v92, v89 row_shr:1 row_mask:0xf bank_mask:0xf
	v_cndmask_b32_e64 v96, v1, 0, s[2:3]
	v_mov_b32_e32 v97, v89
	v_accvgpr_read_b32 v1, a31
	v_pk_fma_f32 v[74:75], v[74:75], v[34:35], v[84:85]
	v_pk_mul_f32 v[84:85], v[96:97], v[92:93]
	v_accvgpr_write_b32 a8, v62
	v_cndmask_b32_e64 v56, v1, 0, s[0:1]
	v_accvgpr_read_b32 v1, a15
	v_pk_fma_f32 v[84:85], v[88:89], v[62:63], v[84:85] op_sel_hi:[0,1,1]
	v_accvgpr_write_b32 a9, v63
	v_cndmask_b32_e64 v62, v1, 0, s[0:1]
	v_accvgpr_read_b32 v1, a7
	v_cndmask_b32_e64 v63, v1, 0, s[0:1]
	v_accvgpr_read_b32 v1, a19
	v_pk_add_f32 v[80:81], v[80:81], 0 op_sel_hi:[1,0]
	v_mov_b32_dpp v59, v88 row_shl:1 row_mask:0xf bank_mask:0xf
	v_pk_mov_b32 v[88:89], v[88:89], v[4:5] op_sel:[1,0]
	v_cndmask_b32_e64 v95, v1, 0, s[0:1]
	v_accvgpr_read_b32 v1, a3
	v_accvgpr_write_b32 a36, v104
	v_pk_add_f32 v[80:81], v[80:81], v[74:75]
	v_pk_fma_f32 v[84:85], v[88:89], v[58:59], v[84:85]
	v_mov_b32_e32 v94, v57
	v_cndmask_b32_e64 v98, v1, 0, s[8:9]
	v_accvgpr_read_b32 v1, a11
	v_accvgpr_write_b32 a37, v105
	v_accvgpr_write_b32 a32, v102
	v_pk_add_f32 v[80:81], v[80:81], v[84:85]
	s_mov_b64 s[4:5], 0x20000
	v_mov_b32_dpp v94, v101 row_shr:1 row_mask:0xf bank_mask:0xf
	v_mov_b32_e32 v99, v101
	v_cndmask_b32_e64 v104, v1, 0, s[2:3]
	v_accvgpr_read_b32 v1, a59
	v_accvgpr_write_b32 a29, v15
	v_accvgpr_write_b32 a33, v103
	v_accvgpr_write_b32 a49, v5
	v_lshl_add_u64 v[84:85], v[54:55], 0, s[4:5]
	v_mov_b32_e32 v128, v80
	v_mov_b32_e32 v129, v81
	v_pk_mul_f32 v[80:81], v[98:99], v[94:95]
	v_mov_b32_e32 v102, v51
	v_cndmask_b32_e32 v48, 0, v1, vcc
	v_accvgpr_read_b32 v1, a51
	v_accvgpr_write_b32 a48, v4
	v_mov_b32_dpp v57, v100 row_shl:1 row_mask:0xf bank_mask:0xf
	v_pk_fma_f32 v[80:81], v[100:101], v[62:63], v[80:81] op_sel_hi:[0,1,1]
	v_mov_b32_e32 v84, v101
	v_accvgpr_read_b32 v85, a29
	v_accvgpr_read_b32 v103, a39
	v_mov_b32_dpp v102, v107 row_shr:1 row_mask:0xf bank_mask:0xf
	v_mov_b32_e32 v105, v107
	v_cndmask_b32_e32 v4, 0, v1, vcc
	v_accvgpr_read_b32 v1, a43
	v_pk_fma_f32 v[80:81], v[84:85], v[56:57], v[80:81]
	v_accvgpr_read_b32 v30, a27
	v_accvgpr_read_b32 v31, a23
	v_pk_mul_f32 v[84:85], v[104:105], v[102:103]
	v_cndmask_b32_e32 v5, 0, v1, vcc
	v_accvgpr_read_b32 v1, a35
	v_accvgpr_read_b32 v50, a47
	v_mov_b32_dpp v51, v106 row_shl:1 row_mask:0xf bank_mask:0xf
	v_pk_fma_f32 v[84:85], v[106:107], v[30:31], v[84:85] op_sel_hi:[0,1,1]
	v_mov_b32_e32 v106, v107
	v_mov_b32_e32 v107, v9
	v_cndmask_b32_e32 v1, 0, v1, vcc
	v_accvgpr_read_b32 v2, a55
	v_mov_b32_e32 v108, v49
	v_pk_fma_f32 v[84:85], v[106:107], v[50:51], v[84:85]
	v_pk_add_f32 v[80:81], v[80:81], 0 op_sel_hi:[1,0]
	v_cndmask_b32_e32 v109, 0, v2, vcc
	v_mov_b32_dpp v108, v121 row_shr:1 row_mask:0xf bank_mask:0xf
	v_cndmask_b32_e64 v110, v1, 0, s[2:3]
	v_mov_b32_e32 v111, v121
	v_pk_add_f32 v[80:81], v[80:81], v[84:85]
	v_pk_mul_f32 v[84:85], v[110:111], v[108:109]
	v_mov_b32_dpp v49, v120 row_shl:1 row_mask:0xf bank_mask:0xf
	v_pk_fma_f32 v[84:85], v[120:121], v[4:5], v[84:85] op_sel_hi:[0,1,1]
	v_mov_b32_e32 v120, v121
	v_accvgpr_read_b32 v121, a49
	v_pk_fma_f32 v[84:85], v[120:121], v[48:49], v[84:85]
	s_mov_b64 s[0:1], 0x30000
	v_pk_add_f32 v[80:81], v[80:81], v[84:85]
	v_lshl_add_u64 v[136:137], v[134:135], 0, s[0:1]
	v_add_u32_e32 v1, s17, v118
	s_add_u32 s0, s10, 0x1400000
	s_mov_b64 s[32:33], vcc
	s_nop 1
	s_mov_b64 vcc, s[28:29]
	s_nop 0
	v_cndmask_b32_dpp v130, v80, v128, vcc quad_perm:[1,0,3,2] row_mask:0xf bank_mask:0xf
	v_cndmask_b32_dpp v131, v81, v129, vcc quad_perm:[1,0,3,2] row_mask:0xf bank_mask:0xf
	s_mov_b64 vcc, s[30:31]
	s_nop 0
	v_cndmask_b32_dpp v132, v128, v80, vcc quad_perm:[1,0,3,2] row_mask:0xf bank_mask:0xf
	v_cndmask_b32_dpp v133, v129, v81, vcc quad_perm:[1,0,3,2] row_mask:0xf bank_mask:0xf
	global_store_dwordx4 v[136:137], v[130:133], off sc0 sc1 nt
	s_nop 1
	s_mov_b64 vcc, s[32:33]
	v_readfirstlane_b32 s2, v1
	s_addc_u32 s1, s11, 0
	v_add_u32_e32 v1, s17, v90
	s_waitcnt vmcnt(14)
	v_lshl_add_u64 v[80:81], s[0:1], 0, v[72:73]
	s_mov_b32 m0, s2
	v_readfirstlane_b32 s2, v1
	v_mov_b64_e32 v[74:75], v[82:83]
	v_add_u32_e32 v1, s17, v91
	s_waitcnt lgkmcnt(0)
	s_barrier
	global_load_lds_dwordx4 v[80:81], off nt
	v_lshl_add_u64 v[80:81], s[0:1], 0, v[74:75]
	s_mov_b32 m0, s2
	v_readfirstlane_b32 s2, v1
	v_add_u32_e32 v1, s17, v119
	global_load_lds_dwordx4 v[80:81], off nt
	v_lshl_add_u64 v[80:81], s[0:1], 0, v[124:125]
	s_mov_b32 m0, s2
	v_readfirstlane_b32 s2, v1
	global_load_lds_dwordx4 v[80:81], off nt
	v_lshl_add_u64 v[80:81], s[0:1], 0, v[126:127]
	s_mov_b32 m0, s2
	v_accvgpr_write_b32 a53, v33
	v_accvgpr_write_b32 a2, v62
	v_accvgpr_write_b32 a7, v5
	v_accvgpr_write_b32 a22, v124
	v_accvgpr_write_b32 a30, v126
	global_load_lds_dwordx4 v[80:81], off nt
	v_accvgpr_write_b32 a52, v32
	v_accvgpr_write_b32 a3, v63
	v_accvgpr_write_b32 a6, v4
	v_mov_b64_e32 v[32:33], v[72:73]
	v_accvgpr_write_b32 a23, v125
	v_accvgpr_write_b32 a31, v127
	v_add_u32_e32 v2, 0x1d010, v122
	v_accvgpr_write_b32 a10, v122
	v_add_u32_e32 v5, 0x1d000, v60
	v_mov_b32_e32 v4, v60
	ds_read_b64 v[62:63], v2
	ds_read_b64 v[60:61], v2 offset:288
	ds_read_b64 v[72:73], v2 offset:576
	ds_read_b64 v[70:71], v2 offset:1728
	ds_read_b64 v[68:69], v2 offset:2016
	ds_read_b64 v[82:83], v2 offset:2304
	ds_read_b64 v[80:81], v2 offset:3456
	ds_read_b64 v[84:85], v2 offset:3744
	ds_read_b64 v[126:127], v2 offset:4032
	ds_read_b64 v[124:125], v2 offset:5184
	ds_read_b64 v[122:123], v2 offset:5472
	ds_read_b64 v[120:121], v2 offset:5760
	ds_read_b32 v43, v5
	ds_read_b32 v19, v5 offset:288
	ds_read_b32 v39, v5 offset:576
	ds_read_b32 v25, v5 offset:1728
	ds_read_b32 v7, v5 offset:2016
	ds_read_b32 v21, v5 offset:2304
	ds_read_b32 v11, v5 offset:3456
	ds_read_b32 v35, v5 offset:3744
	ds_read_b32 v59, v5 offset:4032
	ds_read_b32 v57, v5 offset:5184
	ds_read_b32 v51, v5 offset:5472
	ds_read_b32 v49, v5 offset:5760
	s_waitcnt lgkmcnt(0)
	v_mov_b64_e32 v[100:101], v[86:87]
	v_mov_b32_e32 v46, v43
	v_mov_b32_e32 v113, v63
	v_mov_b32_e32 v26, v19
	v_mov_b32_dpp v46, v63 row_shr:1 row_mask:0xf bank_mask:0xf
	v_pk_mul_f32 v[88:89], v[112:113], v[46:47]
	v_mov_b32_dpp v43, v62 row_shl:1 row_mask:0xf bank_mask:0xf
	v_pk_fma_f32 v[88:89], v[62:63], v[116:117], v[88:89] op_sel_hi:[0,1,1]
	v_pk_mov_b32 v[62:63], v[62:63], v[100:101] op_sel:[1,0]
	v_mov_b32_dpp v26, v61 row_shr:1 row_mask:0xf bank_mask:0xf
	v_mov_b32_e32 v17, v61
	v_pk_fma_f32 v[62:63], v[62:63], v[42:43], v[88:89]
	v_pk_mul_f32 v[88:89], v[16:17], v[26:27]
	v_accvgpr_write_b32 a34, v16
	v_accvgpr_read_b32 v16, a52
	v_accvgpr_read_b32 v17, a53
	v_mov_b32_dpp v19, v60 row_shl:1 row_mask:0xf bank_mask:0xf
	v_pk_fma_f32 v[88:89], v[60:61], v[114:115], v[88:89] op_sel_hi:[0,1,1]
	v_pk_mov_b32 v[60:61], v[60:61], v[16:17] op_sel:[1,0]
	v_mov_b32_e32 v44, v39
	v_accvgpr_write_b32 a28, v14
	v_pk_fma_f32 v[60:61], v[60:61], v[18:19], v[88:89]
	v_pk_add_f32 v[62:63], v[62:63], 0 op_sel_hi:[1,0]
	v_mov_b32_dpp v44, v73 row_shr:1 row_mask:0xf bank_mask:0xf
	v_mov_b32_e32 v1, v73
	v_accvgpr_read_b32 v14, a44
	v_accvgpr_read_b32 v89, a21
	v_pk_add_f32 v[60:61], v[62:63], v[60:61]
	v_pk_mul_f32 v[62:63], v[0:1], v[44:45]
	v_accvgpr_read_b32 v15, a45
	v_accvgpr_read_b32 v88, a20
	v_mov_b32_dpp v39, v72 row_shl:1 row_mask:0xf bank_mask:0xf
	v_pk_fma_f32 v[62:63], v[72:73], v[14:15], v[62:63] op_sel_hi:[0,1,1]
	v_pk_mov_b32 v[72:73], v[72:73], v[88:89] op_sel:[1,0]
	v_mov_b32_e32 v36, v25
	v_pk_fma_f32 v[62:63], v[72:73], v[38:39], v[62:63]
	s_mov_b64 s[0:1], 0x400000
	v_pk_add_f32 v[60:61], v[60:61], v[62:63]
	v_mov_b32_dpp v36, v71 row_shr:1 row_mask:0xf bank_mask:0xf
	v_mov_b32_e32 v65, v71
	v_accvgpr_read_b32 v87, a41
	v_lshl_add_u64 v[62:63], v[54:55], 0, s[0:1]
	v_mov_b32_e32 v128, v60
	v_mov_b32_e32 v129, v61
	v_pk_mul_f32 v[60:61], v[64:65], v[36:37]
	v_accvgpr_read_b32 v86, a40
	v_mov_b32_e32 v12, v7
	v_mov_b32_dpp v25, v70 row_shl:1 row_mask:0xf bank_mask:0xf
	v_pk_fma_f32 v[60:61], v[70:71], v[86:87], v[60:61] op_sel_hi:[0,1,1]
	v_mov_b32_e32 v62, v71
	v_mov_b32_e32 v63, v101
	v_mov_b32_dpp v12, v69 row_shr:1 row_mask:0xf bank_mask:0xf
	v_mov_b32_e32 v29, v69
	v_accvgpr_read_b32 v107, a37
	v_pk_fma_f32 v[60:61], v[62:63], v[24:25], v[60:61]
	v_pk_mul_f32 v[62:63], v[28:29], v[12:13]
	v_accvgpr_read_b32 v106, a36
	v_mov_b32_dpp v7, v68 row_shl:1 row_mask:0xf bank_mask:0xf
	v_pk_fma_f32 v[62:63], v[68:69], v[106:107], v[62:63] op_sel_hi:[0,1,1]
	v_mov_b32_e32 v68, v69
	v_mov_b32_e32 v69, v17
	v_mov_b32_e32 v78, v21
	v_pk_fma_f32 v[62:63], v[68:69], v[6:7], v[62:63]
	v_pk_add_f32 v[60:61], v[60:61], 0 op_sel_hi:[1,0]
	v_mov_b32_dpp v78, v83 row_shr:1 row_mask:0xf bank_mask:0xf
	v_mov_b32_e32 v53, v83
	v_accvgpr_read_b32 v14, a24
	v_pk_add_f32 v[60:61], v[60:61], v[62:63]
	v_pk_mul_f32 v[62:63], v[52:53], v[78:79]
	v_accvgpr_read_b32 v15, a25
	v_mov_b32_dpp v21, v82 row_shl:1 row_mask:0xf bank_mask:0xf
	v_pk_fma_f32 v[62:63], v[82:83], v[14:15], v[62:63] op_sel_hi:[0,1,1]
	v_mov_b32_e32 v68, v83
	v_mov_b32_e32 v69, v89
	v_pk_fma_f32 v[62:63], v[68:69], v[20:21], v[62:63]
	v_mov_b32_e32 v76, v11
	v_pk_add_f32 v[60:61], v[60:61], v[62:63]
	s_mov_b64 s[0:1], 0x410000
	v_mov_b32_dpp v76, v81 row_shr:1 row_mask:0xf bank_mask:0xf
	v_mov_b32_e32 v41, v81
	v_lshl_add_u64 v[136:137], v[134:135], 0, s[0:1]
	s_nop 1
	s_mov_b64 vcc, s[28:29]
	s_nop 0
	v_cndmask_b32_dpp v130, v60, v128, vcc quad_perm:[1,0,3,2] row_mask:0xf bank_mask:0xf
	v_cndmask_b32_dpp v131, v61, v129, vcc quad_perm:[1,0,3,2] row_mask:0xf bank_mask:0xf
	s_mov_b64 vcc, s[30:31]
	s_nop 0
	v_cndmask_b32_dpp v132, v128, v60, vcc quad_perm:[1,0,3,2] row_mask:0xf bank_mask:0xf
	v_cndmask_b32_dpp v133, v129, v61, vcc quad_perm:[1,0,3,2] row_mask:0xf bank_mask:0xf
	global_store_dwordx4 v[136:137], v[130:133], off sc0 sc1 nt
	s_nop 1
	v_pk_mul_f32 v[60:61], v[40:41], v[76:77]
	v_accvgpr_write_b32 a36, v66
	v_pk_fma_f32 v[60:61], v[80:81], v[66:67], v[60:61] op_sel_hi:[0,1,1]
	v_accvgpr_write_b32 a37, v67
	v_accvgpr_read_b32 v67, a29
	v_accvgpr_write_b32 a5, v2
	v_accvgpr_write_b32 a38, v100
	v_accvgpr_read_b32 v66, a28
	v_mov_b32_e32 v2, v35
	v_accvgpr_write_b32 a39, v101
	v_mov_b32_dpp v11, v80 row_shl:1 row_mask:0xf bank_mask:0xf
	v_pk_mov_b32 v[62:63], v[80:81], v[66:67] op_sel:[1,0]
	v_mov_b32_dpp v2, v85 row_shr:1 row_mask:0xf bank_mask:0xf
	v_mov_b32_e32 v23, v85
	v_accvgpr_read_b32 v101, a33
	v_pk_fma_f32 v[60:61], v[62:63], v[10:11], v[60:61]
	v_pk_mul_f32 v[62:63], v[22:23], v[2:3]
	v_accvgpr_read_b32 v100, a32
	v_mov_b32_dpp v35, v84 row_shl:1 row_mask:0xf bank_mask:0xf
	v_pk_fma_f32 v[62:63], v[84:85], v[100:101], v[62:63] op_sel_hi:[0,1,1]
	v_pk_mov_b32 v[68:69], v[84:85], v[8:9] op_sel:[1,0]
	v_mov_b32_e32 v92, v59
	v_pk_fma_f32 v[62:63], v[68:69], v[34:35], v[62:63]
	v_pk_add_f32 v[60:61], v[60:61], 0 op_sel_hi:[1,0]
	v_mov_b32_dpp v92, v127 row_shr:1 row_mask:0xf bank_mask:0xf
	v_mov_b32_e32 v97, v127
	v_accvgpr_read_b32 v17, a9
	v_accvgpr_read_b32 v71, a49
	v_pk_add_f32 v[60:61], v[60:61], v[62:63]
	v_pk_mul_f32 v[62:63], v[96:97], v[92:93]
	v_accvgpr_read_b32 v16, a8
	v_accvgpr_read_b32 v70, a48
	v_mov_b32_dpp v59, v126 row_shl:1 row_mask:0xf bank_mask:0xf
	v_pk_fma_f32 v[62:63], v[126:127], v[16:17], v[62:63] op_sel_hi:[0,1,1]
	v_pk_mov_b32 v[68:69], v[126:127], v[70:71] op_sel:[1,0]
	v_mov_b32_e32 v94, v57
	v_pk_fma_f32 v[62:63], v[68:69], v[58:59], v[62:63]
	v_accvgpr_write_b32 a20, v28
	v_pk_add_f32 v[60:61], v[60:61], v[62:63]
	s_mov_b64 s[0:1], 0x420000
	v_mov_b32_dpp v94, v125 row_shr:1 row_mask:0xf bank_mask:0xf
	v_mov_b32_e32 v99, v125
	v_accvgpr_read_b32 v29, a3
	v_lshl_add_u64 v[62:63], v[54:55], 0, s[0:1]
	v_mov_b32_e32 v128, v60
	v_mov_b32_e32 v129, v61
	v_pk_mul_f32 v[60:61], v[98:99], v[94:95]
	v_accvgpr_read_b32 v28, a2
	v_mov_b32_e32 v102, v51
	v_mov_b32_dpp v57, v124 row_shl:1 row_mask:0xf bank_mask:0xf
	v_pk_fma_f32 v[60:61], v[124:125], v[28:29], v[60:61] op_sel_hi:[0,1,1]
	v_mov_b32_e32 v62, v125
	v_mov_b32_e32 v63, v67
	v_mov_b32_dpp v102, v123 row_shr:1 row_mask:0xf bank_mask:0xf
	v_mov_b32_e32 v105, v123
	v_pk_fma_f32 v[60:61], v[62:63], v[56:57], v[60:61]
	v_pk_mul_f32 v[62:63], v[104:105], v[102:103]
	v_mov_b32_dpp v51, v122 row_shl:1 row_mask:0xf bank_mask:0xf
	v_pk_fma_f32 v[62:63], v[122:123], v[30:31], v[62:63] op_sel_hi:[0,1,1]
	v_accvgpr_write_b32 a28, v30
	v_mov_b32_e32 v68, v123
	v_mov_b32_e32 v69, v9
	v_mov_b32_e32 v108, v49
	v_accvgpr_write_b32 a29, v31
	v_pk_fma_f32 v[62:63], v[68:69], v[50:51], v[62:63]
	v_pk_add_f32 v[60:61], v[60:61], 0 op_sel_hi:[1,0]
	v_mov_b32_dpp v108, v121 row_shr:1 row_mask:0xf bank_mask:0xf
	v_mov_b32_e32 v111, v121
	v_accvgpr_read_b32 v31, a7
	v_pk_add_f32 v[60:61], v[60:61], v[62:63]
	v_pk_mul_f32 v[62:63], v[110:111], v[108:109]
	v_accvgpr_read_b32 v30, a6
	v_mov_b32_dpp v49, v120 row_shl:1 row_mask:0xf bank_mask:0xf
	v_pk_fma_f32 v[62:63], v[120:121], v[30:31], v[62:63] op_sel_hi:[0,1,1]
	v_mov_b32_e32 v68, v121
	v_mov_b32_e32 v69, v71
	v_pk_fma_f32 v[62:63], v[68:69], v[48:49], v[62:63]
	s_mov_b64 s[0:1], 0x430000
	v_pk_add_f32 v[60:61], v[60:61], v[62:63]
	v_lshl_add_u64 v[136:137], v[134:135], 0, s[0:1]
	v_add_u32_e32 v1, s16, v118
	s_add_u32 s0, s10, 0x1800000
	v_accvgpr_write_b32 a26, v114
	s_nop 1
	s_mov_b64 vcc, s[28:29]
	s_nop 0
	v_cndmask_b32_dpp v130, v60, v128, vcc quad_perm:[1,0,3,2] row_mask:0xf bank_mask:0xf
	v_cndmask_b32_dpp v131, v61, v129, vcc quad_perm:[1,0,3,2] row_mask:0xf bank_mask:0xf
	s_mov_b64 vcc, s[30:31]
	s_nop 0
	v_cndmask_b32_dpp v132, v128, v60, vcc quad_perm:[1,0,3,2] row_mask:0xf bank_mask:0xf
	v_cndmask_b32_dpp v133, v129, v61, vcc quad_perm:[1,0,3,2] row_mask:0xf bank_mask:0xf
	global_store_dwordx4 v[136:137], v[130:133], off sc0 sc1 nt
	s_nop 1
	v_readfirstlane_b32 s2, v1
	s_addc_u32 s1, s11, 0
	v_add_u32_e32 v1, s16, v90
	v_accvgpr_write_b32 a18, v116
	v_accvgpr_write_b32 a27, v115
	s_waitcnt vmcnt(16)
	v_lshl_add_u64 v[60:61], s[0:1], 0, v[32:33]
	s_mov_b32 m0, s2
	v_readfirstlane_b32 s2, v1
	v_add_u32_e32 v1, s16, v91
	v_accvgpr_read_b32 v115, a23
	v_accvgpr_write_b32 a19, v117
	s_waitcnt lgkmcnt(0)
	s_barrier
	global_load_lds_dwordx4 v[60:61], off nt
	v_lshl_add_u64 v[60:61], s[0:1], 0, v[74:75]
	s_mov_b32 m0, s2
	v_readfirstlane_b32 s2, v1
	v_accvgpr_read_b32 v114, a22
	v_add_u32_e32 v1, s16, v119
	v_accvgpr_read_b32 v117, a31
	global_load_lds_dwordx4 v[60:61], off nt
	v_lshl_add_u64 v[60:61], s[0:1], 0, v[114:115]
	s_mov_b32 m0, s2
	v_readfirstlane_b32 s2, v1
	v_accvgpr_read_b32 v116, a30
	global_load_lds_dwordx4 v[60:61], off nt
	v_lshl_add_u64 v[60:61], s[0:1], 0, v[116:117]
	s_mov_b32 m0, s2
	v_accvgpr_write_b32 a1, v5
	global_load_lds_dwordx4 v[60:61], off nt
	v_accvgpr_read_b32 v5, a10
	v_add_u32_e32 v2, 16, v5
	ds_read_b64 v[60:61], v2
	ds_read_b64 v[62:63], v2 offset:288
	ds_read_b64 v[68:69], v2 offset:576
	ds_read_b64 v[70:71], v2 offset:1728
	ds_read_b64 v[72:73], v2 offset:2016
	ds_read_b64 v[82:83], v2 offset:2304
	ds_read_b64 v[80:81], v2 offset:3456
	ds_read_b64 v[84:85], v2 offset:3744
	ds_read_b64 v[124:125], v2 offset:4032
	ds_read_b64 v[122:123], v2 offset:5184
	ds_read_b64 v[120:121], v2 offset:5472
	ds_read_b64 v[90:91], v2 offset:5760
	ds_read_b32 v43, v4
	ds_read_b32 v19, v4 offset:288
	ds_read_b32 v39, v4 offset:576
	ds_read_b32 v25, v4 offset:1728
	ds_read_b32 v7, v4 offset:2016
	ds_read_b32 v21, v4 offset:2304
	ds_read_b32 v11, v4 offset:3456
	ds_read_b32 v35, v4 offset:3744
	ds_read_b32 v59, v4 offset:4032
	ds_read_b32 v57, v4 offset:5184
	ds_read_b32 v51, v4 offset:5472
	ds_read_b32 v49, v4 offset:5760
	s_waitcnt lgkmcnt(0)
	v_accvgpr_write_b32 a46, v88
	v_mov_b32_e32 v46, v43
	v_accvgpr_write_b32 a8, v8
	v_mov_b32_e32 v113, v61
	v_mov_b32_dpp v46, v61 row_shr:1 row_mask:0xf bank_mask:0xf
	v_accvgpr_mov_b32 a42, a52
	v_accvgpr_write_b32 a47, v89
	v_accvgpr_write_b32 a9, v9
	v_pk_mul_f32 v[88:89], v[112:113], v[46:47]
	v_accvgpr_write_b32 a40, v112
	v_accvgpr_read_b32 v8, a18
	v_accvgpr_read_b32 v113, a39
	v_accvgpr_mov_b32 a43, a53
	v_accvgpr_write_b32 a51, v33
	v_accvgpr_write_b32 a52, v74
	v_accvgpr_read_b32 v9, a19
	v_accvgpr_read_b32 v112, a38
	v_mov_b32_e32 v26, v19
	v_accvgpr_write_b32 a50, v32
	v_accvgpr_write_b32 a53, v75
	v_mov_b32_dpp v43, v60 row_shl:1 row_mask:0xf bank_mask:0xf
	v_pk_fma_f32 v[88:89], v[60:61], v[8:9], v[88:89] op_sel_hi:[0,1,1]
	v_pk_mov_b32 v[60:61], v[60:61], v[112:113] op_sel:[1,0]
	v_mov_b32_dpp v26, v63 row_shr:1 row_mask:0xf bank_mask:0xf
	v_accvgpr_read_b32 v32, a34
	v_mov_b32_e32 v33, v63
	v_accvgpr_read_b32 v127, a27
	v_accvgpr_read_b32 v75, a43
	v_pk_fma_f32 v[60:61], v[60:61], v[42:43], v[88:89]
	v_pk_mul_f32 v[88:89], v[32:33], v[26:27]
	v_accvgpr_read_b32 v126, a26
	v_accvgpr_read_b32 v74, a42
	v_mov_b32_dpp v19, v62 row_shl:1 row_mask:0xf bank_mask:0xf
	v_pk_fma_f32 v[88:89], v[62:63], v[126:127], v[88:89] op_sel_hi:[0,1,1]
	v_pk_mov_b32 v[62:63], v[62:63], v[74:75] op_sel:[1,0]
	v_mov_b32_e32 v44, v39
	v_accvgpr_mov_b32 a14, a48
	v_pk_fma_f32 v[62:63], v[62:63], v[18:19], v[88:89]
	v_pk_add_f32 v[60:61], v[60:61], 0 op_sel_hi:[1,0]
	v_mov_b32_dpp v44, v69 row_shr:1 row_mask:0xf bank_mask:0xf
	v_mov_b32_e32 v1, v69
	v_accvgpr_mov_b32 a15, a49
	v_pk_add_f32 v[60:61], v[60:61], v[62:63]
	v_pk_mul_f32 v[62:63], v[0:1], v[44:45]
	v_accvgpr_write_b32 a48, v0
	v_accvgpr_read_b32 v89, a45
	v_accvgpr_read_b32 v0, a46
	v_accvgpr_read_b32 v88, a44
	v_accvgpr_read_b32 v1, a47
	v_mov_b32_dpp v39, v68 row_shl:1 row_mask:0xf bank_mask:0xf
	v_pk_fma_f32 v[62:63], v[68:69], v[88:89], v[62:63] op_sel_hi:[0,1,1]
	v_pk_mov_b32 v[68:69], v[68:69], v[0:1] op_sel:[1,0]
	v_mov_b32_e32 v36, v25
	v_pk_fma_f32 v[62:63], v[68:69], v[38:39], v[62:63]
	s_mov_b64 s[0:1], 0x800000
	v_pk_add_f32 v[60:61], v[60:61], v[62:63]
	v_mov_b32_dpp v36, v71 row_shr:1 row_mask:0xf bank_mask:0xf
	v_mov_b32_e32 v65, v71
	v_lshl_add_u64 v[62:63], v[54:55], 0, s[0:1]
	v_mov_b32_e32 v128, v60
	v_mov_b32_e32 v129, v61
	v_pk_mul_f32 v[60:61], v[64:65], v[36:37]
	v_mov_b64_e32 v[118:119], v[86:87]
	v_mov_b32_e32 v12, v7
	v_accvgpr_write_b32 a24, v32
	v_mov_b32_dpp v25, v70 row_shl:1 row_mask:0xf bank_mask:0xf
	v_pk_fma_f32 v[60:61], v[70:71], v[118:119], v[60:61] op_sel_hi:[0,1,1]
	v_mov_b32_e32 v62, v71
	v_mov_b32_e32 v63, v113
	v_mov_b32_dpp v12, v73 row_shr:1 row_mask:0xf bank_mask:0xf
	v_accvgpr_read_b32 v32, a20
	v_mov_b32_e32 v33, v73
	v_pk_fma_f32 v[60:61], v[62:63], v[24:25], v[60:61]
	v_pk_mul_f32 v[62:63], v[32:33], v[12:13]
	v_mov_b32_dpp v7, v72 row_shl:1 row_mask:0xf bank_mask:0xf
	v_pk_fma_f32 v[62:63], v[72:73], v[106:107], v[62:63] op_sel_hi:[0,1,1]
	v_mov_b32_e32 v68, v73
	v_mov_b32_e32 v69, v75
	v_mov_b32_e32 v78, v21
	v_pk_fma_f32 v[62:63], v[68:69], v[6:7], v[62:63]
	v_pk_add_f32 v[60:61], v[60:61], 0 op_sel_hi:[1,0]
	v_mov_b32_dpp v78, v83 row_shr:1 row_mask:0xf bank_mask:0xf
	v_mov_b32_e32 v53, v83
	v_pk_add_f32 v[60:61], v[60:61], v[62:63]
	v_pk_mul_f32 v[62:63], v[52:53], v[78:79]
	v_mov_b32_dpp v21, v82 row_shl:1 row_mask:0xf bank_mask:0xf
	v_pk_fma_f32 v[62:63], v[82:83], v[14:15], v[62:63] op_sel_hi:[0,1,1]
	v_mov_b32_e32 v68, v83
	v_mov_b32_e32 v69, v1
	v_accvgpr_write_b32 a19, v15
	v_pk_fma_f32 v[62:63], v[68:69], v[20:21], v[62:63]
	v_mov_b32_e32 v76, v11
	v_accvgpr_write_b32 a18, v14
	v_pk_add_f32 v[60:61], v[60:61], v[62:63]
	s_mov_b64 s[0:1], 0x810000
	v_mov_b32_dpp v76, v81 row_shr:1 row_mask:0xf bank_mask:0xf
	v_mov_b32_e32 v41, v81
	v_accvgpr_read_b32 v14, a36
	v_accvgpr_write_b32 a6, v2
	v_lshl_add_u64 v[136:137], v[134:135], 0, s[0:1]
	s_nop 1
	s_mov_b64 vcc, s[28:29]
	s_nop 0
	v_cndmask_b32_dpp v130, v60, v128, vcc quad_perm:[1,0,3,2] row_mask:0xf bank_mask:0xf
	v_cndmask_b32_dpp v131, v61, v129, vcc quad_perm:[1,0,3,2] row_mask:0xf bank_mask:0xf
	s_mov_b64 vcc, s[30:31]
	s_nop 0
	v_cndmask_b32_dpp v132, v128, v60, vcc quad_perm:[1,0,3,2] row_mask:0xf bank_mask:0xf
	v_cndmask_b32_dpp v133, v129, v61, vcc quad_perm:[1,0,3,2] row_mask:0xf bank_mask:0xf
	global_store_dwordx4 v[136:137], v[130:133], off sc0 sc1 nt
	s_nop 1
	v_pk_mul_f32 v[60:61], v[40:41], v[76:77]
	v_accvgpr_read_b32 v15, a37
	v_mov_b32_e32 v2, v35
	v_mov_b32_dpp v11, v80 row_shl:1 row_mask:0xf bank_mask:0xf
	v_pk_fma_f32 v[60:61], v[80:81], v[14:15], v[60:61] op_sel_hi:[0,1,1]
	v_pk_mov_b32 v[62:63], v[80:81], v[66:67] op_sel:[1,0]
	v_mov_b32_dpp v2, v85 row_shr:1 row_mask:0xf bank_mask:0xf
	v_mov_b32_e32 v23, v85
	v_accvgpr_read_b32 v15, a9
	v_pk_fma_f32 v[60:61], v[62:63], v[10:11], v[60:61]
	v_pk_mul_f32 v[62:63], v[22:23], v[2:3]
	v_accvgpr_read_b32 v14, a8
	v_mov_b32_dpp v35, v84 row_shl:1 row_mask:0xf bank_mask:0xf
	v_pk_fma_f32 v[62:63], v[84:85], v[100:101], v[62:63] op_sel_hi:[0,1,1]
	v_pk_mov_b32 v[68:69], v[84:85], v[14:15] op_sel:[1,0]
	v_mov_b32_e32 v92, v59
	v_pk_fma_f32 v[62:63], v[68:69], v[34:35], v[62:63]
	v_pk_add_f32 v[60:61], v[60:61], 0 op_sel_hi:[1,0]
	v_mov_b32_dpp v92, v125 row_shr:1 row_mask:0xf bank_mask:0xf
	v_mov_b32_e32 v97, v125
	v_accvgpr_read_b32 v71, a15
	v_pk_add_f32 v[60:61], v[60:61], v[62:63]
	v_pk_mul_f32 v[62:63], v[96:97], v[92:93]
	v_accvgpr_read_b32 v70, a14
	v_mov_b32_dpp v59, v124 row_shl:1 row_mask:0xf bank_mask:0xf
	v_pk_fma_f32 v[62:63], v[124:125], v[16:17], v[62:63] op_sel_hi:[0,1,1]
	v_pk_mov_b32 v[68:69], v[124:125], v[70:71] op_sel:[1,0]
	v_mov_b32_e32 v94, v57
	v_pk_fma_f32 v[62:63], v[68:69], v[58:59], v[62:63]
	s_mov_b64 s[0:1], 0x820000
	v_pk_add_f32 v[60:61], v[60:61], v[62:63]
	v_mov_b32_dpp v94, v123 row_shr:1 row_mask:0xf bank_mask:0xf
	v_mov_b32_e32 v99, v123
	v_accvgpr_write_b32 a31, v17
	v_lshl_add_u64 v[62:63], v[54:55], 0, s[0:1]
	v_mov_b32_e32 v128, v60
	v_mov_b32_e32 v129, v61
	v_pk_mul_f32 v[60:61], v[98:99], v[94:95]
	v_mov_b32_e32 v102, v51
	v_accvgpr_write_b32 a30, v16
	v_mov_b32_dpp v57, v122 row_shl:1 row_mask:0xf bank_mask:0xf
	v_pk_fma_f32 v[60:61], v[122:123], v[28:29], v[60:61] op_sel_hi:[0,1,1]
	v_mov_b32_e32 v62, v123
	v_mov_b32_e32 v63, v67
	v_mov_b32_dpp v102, v121 row_shr:1 row_mask:0xf bank_mask:0xf
	v_mov_b32_e32 v105, v121
	v_accvgpr_read_b32 v16, a28
	v_pk_fma_f32 v[60:61], v[62:63], v[56:57], v[60:61]
	v_pk_mul_f32 v[62:63], v[104:105], v[102:103]
	v_accvgpr_read_b32 v17, a29
	v_mov_b32_dpp v51, v120 row_shl:1 row_mask:0xf bank_mask:0xf
	v_pk_fma_f32 v[62:63], v[120:121], v[16:17], v[62:63] op_sel_hi:[0,1,1]
	v_mov_b32_e32 v68, v121
	v_mov_b32_e32 v69, v15
	v_mov_b32_e32 v108, v49
	v_pk_fma_f32 v[62:63], v[68:69], v[50:51], v[62:63]
	v_pk_add_f32 v[60:61], v[60:61], 0 op_sel_hi:[1,0]
	v_mov_b32_dpp v108, v91 row_shr:1 row_mask:0xf bank_mask:0xf
	v_mov_b32_e32 v111, v91
	v_pk_add_f32 v[60:61], v[60:61], v[62:63]
	v_pk_mul_f32 v[62:63], v[110:111], v[108:109]
	v_mov_b32_dpp v49, v90 row_shl:1 row_mask:0xf bank_mask:0xf
	v_pk_fma_f32 v[62:63], v[90:91], v[30:31], v[62:63] op_sel_hi:[0,1,1]
	v_mov_b32_e32 v68, v91
	v_mov_b32_e32 v69, v71
	v_pk_fma_f32 v[62:63], v[68:69], v[48:49], v[62:63]
	s_mov_b64 s[0:1], 0x830000
	v_mov_b32_e32 v0, v22
	v_pk_add_f32 v[60:61], v[60:61], v[62:63]
	v_lshl_add_u64 v[136:137], v[134:135], 0, s[0:1]
	s_add_u32 s0, s10, 0x1c00000
	v_accvgpr_read_b32 v22, a50
	v_accvgpr_read_b32 v1, a72
	s_addc_u32 s1, s11, 0
	v_accvgpr_read_b32 v23, a51
	s_nop 1
	s_mov_b64 vcc, s[28:29]
	s_nop 0
	v_cndmask_b32_dpp v130, v60, v128, vcc quad_perm:[1,0,3,2] row_mask:0xf bank_mask:0xf
	v_cndmask_b32_dpp v131, v61, v129, vcc quad_perm:[1,0,3,2] row_mask:0xf bank_mask:0xf
	s_mov_b64 vcc, s[30:31]
	s_nop 0
	v_cndmask_b32_dpp v132, v128, v60, vcc quad_perm:[1,0,3,2] row_mask:0xf bank_mask:0xf
	v_cndmask_b32_dpp v133, v129, v61, vcc quad_perm:[1,0,3,2] row_mask:0xf bank_mask:0xf
	global_store_dwordx4 v[136:137], v[130:133], off sc0 sc1 nt
	s_nop 1
	v_readfirstlane_b32 s2, v1
	v_lshl_add_u64 v[60:61], s[0:1], 0, v[22:23]
	v_accvgpr_read_b32 v1, a12
	v_accvgpr_read_b32 v22, a52
	s_waitcnt vmcnt(18)
	s_mov_b32 m0, s2
	v_readfirstlane_b32 s2, v1
	v_accvgpr_read_b32 v23, a53
	v_accvgpr_read_b32 v1, a13
	s_waitcnt lgkmcnt(0)
	s_barrier
	global_load_lds_dwordx4 v[60:61], off nt
	v_lshl_add_u64 v[60:61], s[0:1], 0, v[22:23]
	s_mov_b32 m0, s2
	v_readfirstlane_b32 s2, v1
	v_accvgpr_read_b32 v1, a16
	global_load_lds_dwordx4 v[60:61], off nt
	v_lshl_add_u64 v[60:61], s[0:1], 0, v[114:115]
	s_mov_b32 m0, s2
	v_readfirstlane_b32 s2, v1
	global_load_lds_dwordx4 v[60:61], off nt
	v_lshl_add_u64 v[60:61], s[0:1], 0, v[116:117]
	s_mov_b32 m0, s2
	v_accvgpr_write_b32 a22, v30
	v_accvgpr_write_b32 a44, v70
	global_load_lds_dwordx4 v[60:61], off nt
	v_accvgpr_write_b32 a2, v106
	v_accvgpr_write_b32 a34, v74
	v_accvgpr_write_b32 a23, v31
	v_accvgpr_write_b32 a45, v71
	v_add_u32_e32 v2, 0x7010, v5
	v_mov_b32_e32 v31, v5
	v_add_u32_e32 v5, 0x7000, v4
	ds_read_b64 v[60:61], v2
	ds_read_b64 v[62:63], v2 offset:288
	ds_read_b64 v[68:69], v2 offset:576
	ds_read_b64 v[70:71], v2 offset:1728
	ds_read_b64 v[72:73], v2 offset:2016
	ds_read_b64 v[82:83], v2 offset:2304
	ds_read_b64 v[80:81], v2 offset:3456
	ds_read_b64 v[84:85], v2 offset:3744
	ds_read_b64 v[116:117], v2 offset:4032
	ds_read_b64 v[114:115], v2 offset:5184
	ds_read_b64 v[112:113], v2 offset:5472
	ds_read_b64 v[90:91], v2 offset:5760
	ds_read_b32 v43, v5
	ds_read_b32 v19, v5 offset:288
	ds_read_b32 v39, v5 offset:576
	ds_read_b32 v25, v5 offset:1728
	ds_read_b32 v7, v5 offset:2016
	ds_read_b32 v21, v5 offset:2304
	ds_read_b32 v11, v5 offset:3456
	ds_read_b32 v35, v5 offset:3744
	ds_read_b32 v59, v5 offset:4032
	ds_read_b32 v57, v5 offset:5184
	ds_read_b32 v51, v5 offset:5472
	ds_read_b32 v49, v5 offset:5760
	s_waitcnt lgkmcnt(0)
	v_accvgpr_write_b32 a3, v107
	v_mov_b32_e32 v46, v43
	v_accvgpr_write_b32 a35, v75
	v_accvgpr_read_b32 v74, a40
	v_mov_b32_dpp v46, v61 row_shr:1 row_mask:0xf bank_mask:0xf
	v_mov_b32_e32 v75, v61
	v_accvgpr_read_b32 v107, a39
	v_accvgpr_write_b32 a10, v100
	v_pk_mul_f32 v[86:87], v[74:75], v[46:47]
	v_accvgpr_read_b32 v106, a38
	v_mov_b32_e32 v26, v19
	v_accvgpr_write_b32 a11, v101
	v_mov_b32_dpp v43, v60 row_shl:1 row_mask:0xf bank_mask:0xf
	v_mov_b32_e32 v32, v74
	v_pk_fma_f32 v[86:87], v[60:61], v[8:9], v[86:87] op_sel_hi:[0,1,1]
	v_pk_mov_b32 v[60:61], v[60:61], v[106:107] op_sel:[1,0]
	v_mov_b32_dpp v26, v63 row_shr:1 row_mask:0xf bank_mask:0xf
	v_accvgpr_read_b32 v74, a24
	v_mov_b32_e32 v75, v63
	v_accvgpr_read_b32 v101, a35
	v_pk_fma_f32 v[60:61], v[60:61], v[42:43], v[86:87]
	v_pk_mul_f32 v[86:87], v[74:75], v[26:27]
	v_accvgpr_read_b32 v100, a34
	v_accvgpr_write_b32 a14, v66
	v_mov_b32_dpp v19, v62 row_shl:1 row_mask:0xf bank_mask:0xf
	v_pk_fma_f32 v[86:87], v[62:63], v[126:127], v[86:87] op_sel_hi:[0,1,1]
	v_pk_mov_b32 v[62:63], v[62:63], v[100:101] op_sel:[1,0]
	v_mov_b32_e32 v44, v39
	v_accvgpr_write_b32 a42, v64
	v_accvgpr_write_b32 a15, v67
	v_mov_b32_e32 v66, v4
	v_pk_fma_f32 v[62:63], v[62:63], v[18:19], v[86:87]
	v_pk_add_f32 v[60:61], v[60:61], 0 op_sel_hi:[1,0]
	v_mov_b32_dpp v44, v69 row_shr:1 row_mask:0xf bank_mask:0xf
	v_accvgpr_read_b32 v64, a48
	v_mov_b32_e32 v65, v69
	v_accvgpr_read_b32 v4, a46
	v_pk_add_f32 v[60:61], v[60:61], v[62:63]
	v_pk_mul_f32 v[62:63], v[64:65], v[44:45]
	v_accvgpr_read_b32 v5, a47
	v_mov_b32_dpp v39, v68 row_shl:1 row_mask:0xf bank_mask:0xf
	v_pk_fma_f32 v[62:63], v[68:69], v[88:89], v[62:63] op_sel_hi:[0,1,1]
	v_pk_mov_b32 v[68:69], v[68:69], v[4:5] op_sel:[1,0]
	v_mov_b32_e32 v36, v25
	v_pk_fma_f32 v[62:63], v[68:69], v[38:39], v[62:63]
	s_mov_b64 s[0:1], 0xc00000
	v_pk_add_f32 v[60:61], v[60:61], v[62:63]
	v_mov_b32_dpp v36, v71 row_shr:1 row_mask:0xf bank_mask:0xf
	v_accvgpr_read_b32 v22, a42
	v_mov_b32_e32 v23, v71
	v_accvgpr_mov_b32 a26, a20
	v_accvgpr_write_b32 a20, v28
	v_lshl_add_u64 v[62:63], v[54:55], 0, s[0:1]
	v_mov_b32_e32 v128, v60
	v_mov_b32_e32 v129, v61
	v_pk_mul_f32 v[60:61], v[22:23], v[36:37]
	v_mov_b32_e32 v12, v7
	v_accvgpr_write_b32 a21, v29
	v_mov_b32_dpp v25, v70 row_shl:1 row_mask:0xf bank_mask:0xf
	v_pk_fma_f32 v[60:61], v[70:71], v[118:119], v[60:61] op_sel_hi:[0,1,1]
	v_mov_b32_e32 v62, v71
	v_mov_b32_e32 v63, v107
	v_mov_b32_dpp v12, v73 row_shr:1 row_mask:0xf bank_mask:0xf
	v_accvgpr_read_b32 v28, a26
	v_mov_b32_e32 v29, v73
	v_accvgpr_read_b32 v121, a3
	v_pk_fma_f32 v[60:61], v[62:63], v[24:25], v[60:61]
	v_pk_mul_f32 v[62:63], v[28:29], v[12:13]
	v_accvgpr_read_b32 v120, a2
	v_mov_b32_dpp v7, v72 row_shl:1 row_mask:0xf bank_mask:0xf
	v_pk_fma_f32 v[62:63], v[72:73], v[120:121], v[62:63] op_sel_hi:[0,1,1]
	v_mov_b32_e32 v68, v73
	v_mov_b32_e32 v69, v101
	v_mov_b32_e32 v78, v21
	v_pk_fma_f32 v[62:63], v[68:69], v[6:7], v[62:63]
	v_pk_add_f32 v[60:61], v[60:61], 0 op_sel_hi:[1,0]
	v_mov_b32_dpp v78, v83 row_shr:1 row_mask:0xf bank_mask:0xf
	v_mov_b32_e32 v53, v83
	v_accvgpr_read_b32 v125, a19
	v_pk_add_f32 v[60:61], v[60:61], v[62:63]
	v_pk_mul_f32 v[62:63], v[52:53], v[78:79]
	v_accvgpr_read_b32 v124, a18
	v_mov_b32_dpp v21, v82 row_shl:1 row_mask:0xf bank_mask:0xf
	v_pk_fma_f32 v[62:63], v[82:83], v[124:125], v[62:63] op_sel_hi:[0,1,1]
	v_mov_b32_e32 v68, v83
	v_mov_b32_e32 v69, v5
	v_pk_fma_f32 v[62:63], v[68:69], v[20:21], v[62:63]
	v_mov_b32_e32 v76, v11
	v_pk_add_f32 v[60:61], v[60:61], v[62:63]
	s_mov_b64 s[0:1], 0xc10000
	v_mov_b32_dpp v76, v81 row_shr:1 row_mask:0xf bank_mask:0xf
	v_mov_b32_e32 v41, v81
	v_accvgpr_read_b32 v123, a37
	v_accvgpr_read_b32 v4, a14
	v_lshl_add_u64 v[136:137], v[134:135], 0, s[0:1]
	s_nop 1
	s_mov_b64 vcc, s[28:29]
	s_nop 0
	v_cndmask_b32_dpp v130, v60, v128, vcc quad_perm:[1,0,3,2] row_mask:0xf bank_mask:0xf
	v_cndmask_b32_dpp v131, v61, v129, vcc quad_perm:[1,0,3,2] row_mask:0xf bank_mask:0xf
	s_mov_b64 vcc, s[30:31]
	s_nop 0
	v_cndmask_b32_dpp v132, v128, v60, vcc quad_perm:[1,0,3,2] row_mask:0xf bank_mask:0xf
	v_cndmask_b32_dpp v133, v129, v61, vcc quad_perm:[1,0,3,2] row_mask:0xf bank_mask:0xf
	global_store_dwordx4 v[136:137], v[130:133], off sc0 sc1 nt
	s_nop 1
	v_pk_mul_f32 v[60:61], v[40:41], v[76:77]
	v_accvgpr_read_b32 v122, a36
	v_accvgpr_read_b32 v5, a15
	v_mov_b32_e32 v2, v35
	v_accvgpr_mov_b32 a32, a24
	v_accvgpr_write_b32 a24, v22
	v_mov_b64_e32 v[22:23], v[118:119]
	v_mov_b32_dpp v11, v80 row_shl:1 row_mask:0xf bank_mask:0xf
	v_pk_fma_f32 v[60:61], v[80:81], v[122:123], v[60:61] op_sel_hi:[0,1,1]
	v_pk_mov_b32 v[62:63], v[80:81], v[4:5] op_sel:[1,0]
	v_mov_b32_dpp v2, v85 row_shr:1 row_mask:0xf bank_mask:0xf
	v_mov_b32_e32 v106, v0
	v_mov_b32_e32 v107, v85
	v_accvgpr_read_b32 v119, a11
	v_pk_fma_f32 v[60:61], v[62:63], v[10:11], v[60:61]
	v_pk_mul_f32 v[62:63], v[106:107], v[2:3]
	v_accvgpr_read_b32 v118, a10
	v_mov_b64_e32 v[100:101], v[14:15]
	v_mov_b32_dpp v35, v84 row_shl:1 row_mask:0xf bank_mask:0xf
	v_pk_fma_f32 v[62:63], v[84:85], v[118:119], v[62:63] op_sel_hi:[0,1,1]
	v_pk_mov_b32 v[68:69], v[84:85], v[100:101] op_sel:[1,0]
	v_mov_b32_e32 v92, v59
	v_accvgpr_write_b32 a26, v52
	v_mov_b32_e32 v74, v40
	v_pk_fma_f32 v[62:63], v[68:69], v[34:35], v[62:63]
	v_pk_add_f32 v[60:61], v[60:61], 0 op_sel_hi:[1,0]
	v_mov_b32_dpp v92, v117 row_shr:1 row_mask:0xf bank_mask:0xf
	v_mov_b32_e32 v97, v117
	v_accvgpr_read_b32 v41, a31
	v_accvgpr_read_b32 v53, a45
	v_pk_add_f32 v[60:61], v[60:61], v[62:63]
	v_pk_mul_f32 v[62:63], v[96:97], v[92:93]
	v_accvgpr_read_b32 v40, a30
	v_accvgpr_read_b32 v52, a44
	v_mov_b32_dpp v59, v116 row_shl:1 row_mask:0xf bank_mask:0xf
	v_pk_fma_f32 v[62:63], v[116:117], v[40:41], v[62:63] op_sel_hi:[0,1,1]
	v_pk_mov_b32 v[68:69], v[116:117], v[52:53] op_sel:[1,0]
	v_mov_b32_e32 v94, v57
	v_pk_fma_f32 v[62:63], v[68:69], v[58:59], v[62:63]
	s_mov_b64 s[0:1], 0xc20000
	v_pk_add_f32 v[60:61], v[60:61], v[62:63]
	v_mov_b32_dpp v94, v115 row_shr:1 row_mask:0xf bank_mask:0xf
	v_mov_b32_e32 v99, v115
	v_accvgpr_read_b32 v14, a20
	v_lshl_add_u64 v[62:63], v[54:55], 0, s[0:1]
	v_mov_b32_e32 v128, v60
	v_mov_b32_e32 v129, v61
	v_pk_mul_f32 v[60:61], v[98:99], v[94:95]
	v_accvgpr_read_b32 v15, a21
	v_mov_b32_e32 v102, v51
	v_mov_b32_dpp v57, v114 row_shl:1 row_mask:0xf bank_mask:0xf
	v_pk_fma_f32 v[60:61], v[114:115], v[14:15], v[60:61] op_sel_hi:[0,1,1]
	v_mov_b32_e32 v62, v115
	v_mov_b32_e32 v63, v5
	v_mov_b32_dpp v102, v113 row_shr:1 row_mask:0xf bank_mask:0xf
	v_mov_b32_e32 v105, v113
	v_pk_fma_f32 v[60:61], v[62:63], v[56:57], v[60:61]
	v_pk_mul_f32 v[62:63], v[104:105], v[102:103]
	v_accvgpr_write_b32 a8, v8
	v_mov_b32_dpp v51, v112 row_shl:1 row_mask:0xf bank_mask:0xf
	v_pk_fma_f32 v[62:63], v[112:113], v[16:17], v[62:63] op_sel_hi:[0,1,1]
	v_mov_b32_e32 v68, v113
	v_mov_b32_e32 v69, v101
	v_mov_b32_e32 v108, v49
	v_accvgpr_write_b32 a9, v9
	v_pk_fma_f32 v[62:63], v[68:69], v[50:51], v[62:63]
	v_pk_add_f32 v[60:61], v[60:61], 0 op_sel_hi:[1,0]
	v_mov_b32_dpp v108, v91 row_shr:1 row_mask:0xf bank_mask:0xf
	v_mov_b32_e32 v111, v91
	v_accvgpr_read_b32 v8, a22
	v_pk_add_f32 v[60:61], v[60:61], v[62:63]
	v_pk_mul_f32 v[62:63], v[110:111], v[108:109]
	v_accvgpr_read_b32 v9, a23
	v_mov_b32_dpp v49, v90 row_shl:1 row_mask:0xf bank_mask:0xf
	v_pk_fma_f32 v[62:63], v[90:91], v[8:9], v[62:63] op_sel_hi:[0,1,1]
	v_mov_b32_e32 v68, v91
	v_mov_b32_e32 v69, v53
	v_pk_fma_f32 v[62:63], v[68:69], v[48:49], v[62:63]
	s_mov_b64 s[0:1], 0xc30000
	v_pk_add_f32 v[60:61], v[60:61], v[62:63]
	v_lshl_add_u64 v[136:137], v[134:135], 0, s[0:1]
	s_nop 1
	s_mov_b64 vcc, s[28:29]
	s_nop 0
	v_cndmask_b32_dpp v130, v60, v128, vcc quad_perm:[1,0,3,2] row_mask:0xf bank_mask:0xf
	v_cndmask_b32_dpp v131, v61, v129, vcc quad_perm:[1,0,3,2] row_mask:0xf bank_mask:0xf
	s_mov_b64 vcc, s[30:31]
	s_nop 0
	v_cndmask_b32_dpp v132, v128, v60, vcc quad_perm:[1,0,3,2] row_mask:0xf bank_mask:0xf
	v_cndmask_b32_dpp v133, v129, v61, vcc quad_perm:[1,0,3,2] row_mask:0xf bank_mask:0xf
	global_store_dwordx4 v[136:137], v[130:133], off sc0 sc1 nt
	s_nop 1
	s_waitcnt vmcnt(20)
	v_accvgpr_write_b32 a16, v88
	v_accvgpr_write_b32 a10, v100
	s_waitcnt lgkmcnt(0)
	s_barrier
	v_add_u32_e32 v2, 0xe010, v31
	v_add_u32_e32 v5, 0xe000, v66
	ds_read_b64 v[60:61], v2
	ds_read_b64 v[62:63], v2 offset:288
	ds_read_b64 v[68:69], v2 offset:576
	ds_read_b64 v[70:71], v2 offset:1728
	ds_read_b64 v[72:73], v2 offset:2016
	ds_read_b64 v[82:83], v2 offset:2304
	ds_read_b64 v[80:81], v2 offset:3456
	ds_read_b64 v[84:85], v2 offset:3744
	ds_read_b64 v[116:117], v2 offset:4032
	ds_read_b64 v[114:115], v2 offset:5184
	ds_read_b64 v[112:113], v2 offset:5472
	ds_read_b64 v[90:91], v2 offset:5760
	ds_read_b32 v43, v5
	ds_read_b32 v19, v5 offset:288
	ds_read_b32 v39, v5 offset:576
	ds_read_b32 v25, v5 offset:1728
	ds_read_b32 v7, v5 offset:2016
	ds_read_b32 v21, v5 offset:2304
	ds_read_b32 v11, v5 offset:3456
	ds_read_b32 v35, v5 offset:3744
	ds_read_b32 v59, v5 offset:4032
	ds_read_b32 v57, v5 offset:5184
	ds_read_b32 v51, v5 offset:5472
	ds_read_b32 v49, v5 offset:5760
	s_waitcnt lgkmcnt(0)
	v_accvgpr_write_b32 a17, v89
	v_mov_b32_e32 v46, v43
	v_accvgpr_write_b32 a11, v101
	v_mov_b32_e32 v33, v61
	v_mov_b32_dpp v46, v61 row_shr:1 row_mask:0xf bank_mask:0xf
	v_accvgpr_read_b32 v89, a9
	v_accvgpr_read_b32 v101, a39
	v_pk_mul_f32 v[86:87], v[32:33], v[46:47]
	v_accvgpr_read_b32 v88, a8
	v_accvgpr_read_b32 v100, a38
	v_mov_b32_e32 v26, v19
	v_accvgpr_write_b32 a19, v17
	v_mov_b32_dpp v43, v60 row_shl:1 row_mask:0xf bank_mask:0xf
	v_pk_fma_f32 v[86:87], v[60:61], v[88:89], v[86:87] op_sel_hi:[0,1,1]
	v_pk_mov_b32 v[60:61], v[60:61], v[100:101] op_sel:[1,0]
	v_mov_b32_dpp v26, v63 row_shr:1 row_mask:0xf bank_mask:0xf
	v_accvgpr_read_b32 v0, a32
	v_mov_b32_e32 v1, v63
	v_accvgpr_read_b32 v4, a34
	v_accvgpr_write_b32 a18, v16
	v_pk_fma_f32 v[60:61], v[60:61], v[42:43], v[86:87]
	v_pk_mul_f32 v[86:87], v[0:1], v[26:27]
	v_mov_b64_e32 v[16:17], v[126:127]
	v_accvgpr_read_b32 v5, a35
	v_mov_b32_dpp v19, v62 row_shl:1 row_mask:0xf bank_mask:0xf
	v_pk_fma_f32 v[86:87], v[62:63], v[16:17], v[86:87] op_sel_hi:[0,1,1]
	v_pk_mov_b32 v[62:63], v[62:63], v[4:5] op_sel:[1,0]
	v_mov_b32_e32 v44, v39
	v_accvgpr_read_b32 v30, a48
	v_mov_b32_e32 v64, v28
	v_accvgpr_write_b32 a7, v66
	v_pk_fma_f32 v[62:63], v[62:63], v[18:19], v[86:87]
	v_pk_add_f32 v[60:61], v[60:61], 0 op_sel_hi:[1,0]
	v_mov_b32_dpp v44, v69 row_shr:1 row_mask:0xf bank_mask:0xf
	v_mov_b32_e32 v31, v69
	v_accvgpr_read_b32 v29, a17
	v_accvgpr_read_b32 v67, a47
	v_pk_add_f32 v[60:61], v[60:61], v[62:63]
	v_pk_mul_f32 v[62:63], v[30:31], v[44:45]
	v_accvgpr_read_b32 v28, a16
	v_accvgpr_read_b32 v66, a46
	v_mov_b32_dpp v39, v68 row_shl:1 row_mask:0xf bank_mask:0xf
	v_pk_fma_f32 v[62:63], v[68:69], v[28:29], v[62:63] op_sel_hi:[0,1,1]
	v_pk_mov_b32 v[68:69], v[68:69], v[66:67] op_sel:[1,0]
	v_mov_b32_e32 v36, v25
	v_pk_fma_f32 v[62:63], v[68:69], v[38:39], v[62:63]
	s_mov_b64 s[0:1], 0x1000000
	v_pk_add_f32 v[60:61], v[60:61], v[62:63]
	v_mov_b32_dpp v36, v71 row_shr:1 row_mask:0xf bank_mask:0xf
	v_accvgpr_read_b32 v126, a24
	v_mov_b32_e32 v127, v71
	v_lshl_add_u64 v[62:63], v[54:55], 0, s[0:1]
	v_mov_b32_e32 v128, v60
	v_mov_b32_e32 v129, v61
	v_pk_mul_f32 v[60:61], v[126:127], v[36:37]
	v_mov_b32_e32 v12, v7
	v_mov_b32_dpp v25, v70 row_shl:1 row_mask:0xf bank_mask:0xf
	v_pk_fma_f32 v[60:61], v[70:71], v[22:23], v[60:61] op_sel_hi:[0,1,1]
	v_mov_b32_e32 v62, v71
	v_mov_b32_e32 v63, v101
	v_mov_b32_dpp v12, v73 row_shr:1 row_mask:0xf bank_mask:0xf
	v_mov_b32_e32 v52, v64
	v_mov_b32_e32 v53, v73
	v_pk_fma_f32 v[60:61], v[62:63], v[24:25], v[60:61]
	v_pk_mul_f32 v[62:63], v[52:53], v[12:13]
	v_mov_b32_dpp v7, v72 row_shl:1 row_mask:0xf bank_mask:0xf
	v_pk_fma_f32 v[62:63], v[72:73], v[120:121], v[62:63] op_sel_hi:[0,1,1]
	v_mov_b32_e32 v68, v73
	v_mov_b32_e32 v69, v5
	v_mov_b32_e32 v78, v21
	v_pk_fma_f32 v[62:63], v[68:69], v[6:7], v[62:63]
	v_pk_add_f32 v[60:61], v[60:61], 0 op_sel_hi:[1,0]
	v_mov_b32_dpp v78, v83 row_shr:1 row_mask:0xf bank_mask:0xf
	v_accvgpr_read_b32 v4, a26
	v_mov_b32_e32 v5, v83
	v_pk_add_f32 v[60:61], v[60:61], v[62:63]
	v_pk_mul_f32 v[62:63], v[4:5], v[78:79]
	v_mov_b32_dpp v21, v82 row_shl:1 row_mask:0xf bank_mask:0xf
	v_pk_fma_f32 v[62:63], v[82:83], v[124:125], v[62:63] op_sel_hi:[0,1,1]
	v_mov_b32_e32 v68, v83
	v_mov_b32_e32 v69, v67
	v_accvgpr_write_b32 a8, v120
	v_pk_fma_f32 v[62:63], v[68:69], v[20:21], v[62:63]
	v_mov_b32_e32 v76, v11
	v_accvgpr_write_b32 a9, v121
	v_pk_add_f32 v[60:61], v[60:61], v[62:63]
	s_mov_b64 s[0:1], 0x1010000
	v_mov_b32_dpp v76, v81 row_shr:1 row_mask:0xf bank_mask:0xf
	v_mov_b32_e32 v120, v74
	v_mov_b32_e32 v121, v81
	v_accvgpr_read_b32 v101, a15
	v_accvgpr_mov_b32 a12, a38
	v_lshl_add_u64 v[136:137], v[134:135], 0, s[0:1]
	s_nop 1
	s_mov_b64 vcc, s[28:29]
	s_nop 0
	v_cndmask_b32_dpp v130, v60, v128, vcc quad_perm:[1,0,3,2] row_mask:0xf bank_mask:0xf
	v_cndmask_b32_dpp v131, v61, v129, vcc quad_perm:[1,0,3,2] row_mask:0xf bank_mask:0xf
	s_mov_b64 vcc, s[30:31]
	s_nop 0
	v_cndmask_b32_dpp v132, v128, v60, vcc quad_perm:[1,0,3,2] row_mask:0xf bank_mask:0xf
	v_cndmask_b32_dpp v133, v129, v61, vcc quad_perm:[1,0,3,2] row_mask:0xf bank_mask:0xf
	global_store_dwordx4 v[136:137], v[130:133], off sc0 sc1 nt
	s_nop 1
	v_pk_mul_f32 v[60:61], v[120:121], v[76:77]
	v_accvgpr_read_b32 v100, a14
	v_mov_b32_e32 v2, v35
	v_accvgpr_mov_b32 a13, a39
	v_accvgpr_write_b32 a20, v22
	v_mov_b32_dpp v11, v80 row_shl:1 row_mask:0xf bank_mask:0xf
	v_pk_fma_f32 v[60:61], v[80:81], v[122:123], v[60:61] op_sel_hi:[0,1,1]
	v_pk_mov_b32 v[62:63], v[80:81], v[100:101] op_sel:[1,0]
	v_mov_b32_dpp v2, v85 row_shr:1 row_mask:0xf bank_mask:0xf
	v_mov_b32_e32 v107, v85
	v_accvgpr_read_b32 v123, a11
	v_accvgpr_write_b32 a21, v23
	v_accvgpr_read_b32 v23, a13
	v_pk_fma_f32 v[60:61], v[62:63], v[10:11], v[60:61]
	v_pk_mul_f32 v[62:63], v[106:107], v[2:3]
	v_accvgpr_read_b32 v122, a10
	v_accvgpr_read_b32 v22, a12
	v_mov_b32_dpp v35, v84 row_shl:1 row_mask:0xf bank_mask:0xf
	v_pk_fma_f32 v[62:63], v[84:85], v[118:119], v[62:63] op_sel_hi:[0,1,1]
	v_accvgpr_write_b32 a12, v118
	v_pk_mov_b32 v[68:69], v[84:85], v[122:123] op_sel:[1,0]
	v_mov_b32_e32 v92, v59
	v_accvgpr_write_b32 a13, v119
	v_pk_fma_f32 v[62:63], v[68:69], v[34:35], v[62:63]
	v_pk_add_f32 v[60:61], v[60:61], 0 op_sel_hi:[1,0]
	v_mov_b32_dpp v92, v117 row_shr:1 row_mask:0xf bank_mask:0xf
	v_mov_b32_e32 v97, v117
	v_mov_b64_e32 v[118:119], v[40:41]
	v_accvgpr_read_b32 v40, a44
	v_pk_add_f32 v[60:61], v[60:61], v[62:63]
	v_pk_mul_f32 v[62:63], v[96:97], v[92:93]
	v_accvgpr_read_b32 v41, a45
	v_mov_b32_dpp v59, v116 row_shl:1 row_mask:0xf bank_mask:0xf
	v_pk_fma_f32 v[62:63], v[116:117], v[118:119], v[62:63] op_sel_hi:[0,1,1]
	v_pk_mov_b32 v[68:69], v[116:117], v[40:41] op_sel:[1,0]
	v_mov_b32_e32 v94, v57
	v_pk_fma_f32 v[62:63], v[68:69], v[58:59], v[62:63]
	s_mov_b64 s[0:1], 0x1020000
	v_pk_add_f32 v[60:61], v[60:61], v[62:63]
	v_mov_b32_dpp v94, v115 row_shr:1 row_mask:0xf bank_mask:0xf
	v_mov_b32_e32 v99, v115
	v_lshl_add_u64 v[62:63], v[54:55], 0, s[0:1]
	v_mov_b32_e32 v128, v60
	v_mov_b32_e32 v129, v61
	v_pk_mul_f32 v[60:61], v[98:99], v[94:95]
	v_mov_b32_e32 v102, v51
	v_accvgpr_write_b32 a30, v4
	v_mov_b32_dpp v57, v114 row_shl:1 row_mask:0xf bank_mask:0xf
	v_pk_fma_f32 v[60:61], v[114:115], v[14:15], v[60:61] op_sel_hi:[0,1,1]
	v_mov_b32_e32 v62, v115
	v_mov_b32_e32 v63, v101
	v_mov_b32_dpp v102, v113 row_shr:1 row_mask:0xf bank_mask:0xf
	v_mov_b32_e32 v105, v113
	v_accvgpr_read_b32 v4, a18
	v_pk_fma_f32 v[60:61], v[62:63], v[56:57], v[60:61]
	v_pk_mul_f32 v[62:63], v[104:105], v[102:103]
	v_accvgpr_read_b32 v5, a19
	v_mov_b32_dpp v51, v112 row_shl:1 row_mask:0xf bank_mask:0xf
	v_pk_fma_f32 v[62:63], v[112:113], v[4:5], v[62:63] op_sel_hi:[0,1,1]
	v_mov_b32_e32 v68, v113
	v_mov_b32_e32 v69, v123
	v_mov_b32_e32 v108, v49
	v_pk_fma_f32 v[62:63], v[68:69], v[50:51], v[62:63]
	v_pk_add_f32 v[60:61], v[60:61], 0 op_sel_hi:[1,0]
	v_mov_b32_dpp v108, v91 row_shr:1 row_mask:0xf bank_mask:0xf
	v_mov_b32_e32 v111, v91
	v_pk_add_f32 v[60:61], v[60:61], v[62:63]
	v_pk_mul_f32 v[62:63], v[110:111], v[108:109]
	v_mov_b32_dpp v49, v90 row_shl:1 row_mask:0xf bank_mask:0xf
	v_pk_fma_f32 v[62:63], v[90:91], v[8:9], v[62:63] op_sel_hi:[0,1,1]
	v_mov_b32_e32 v68, v91
	v_mov_b32_e32 v69, v41
	v_pk_fma_f32 v[62:63], v[68:69], v[48:49], v[62:63]
	s_mov_b64 s[0:1], 0x1030000
	v_pk_add_f32 v[60:61], v[60:61], v[62:63]
	v_lshl_add_u64 v[136:137], v[134:135], 0, s[0:1]
	s_nop 1
	s_mov_b64 vcc, s[28:29]
	s_nop 0
	v_cndmask_b32_dpp v130, v60, v128, vcc quad_perm:[1,0,3,2] row_mask:0xf bank_mask:0xf
	v_cndmask_b32_dpp v131, v61, v129, vcc quad_perm:[1,0,3,2] row_mask:0xf bank_mask:0xf
	s_mov_b64 vcc, s[30:31]
	s_nop 0
	v_cndmask_b32_dpp v132, v128, v60, vcc quad_perm:[1,0,3,2] row_mask:0xf bank_mask:0xf
	v_cndmask_b32_dpp v133, v129, v61, vcc quad_perm:[1,0,3,2] row_mask:0xf bank_mask:0xf
	global_store_dwordx4 v[136:137], v[130:133], off sc0 sc1 nt
	s_nop 1
	s_waitcnt vmcnt(16)
	s_waitcnt lgkmcnt(0)
	s_barrier
	v_accvgpr_read_b32 v2, a0
	v_accvgpr_read_b32 v8, a4
	ds_read_b64 v[60:61], v8
	ds_read_b64 v[62:63], v8 offset:288
	ds_read_b64 v[68:69], v8 offset:576
	ds_read_b64 v[70:71], v8 offset:1728
	ds_read_b64 v[72:73], v8 offset:2016
	ds_read_b64 v[82:83], v8 offset:2304
	ds_read_b64 v[80:81], v8 offset:3456
	ds_read_b64 v[84:85], v8 offset:3744
	ds_read_b64 v[116:117], v8 offset:4032
	ds_read_b64 v[114:115], v8 offset:5184
	ds_read_b64 v[112:113], v8 offset:5472
	ds_read_b64 v[90:91], v8 offset:5760
	ds_read_b32 v43, v2
	ds_read_b32 v19, v2 offset:288
	ds_read_b32 v39, v2 offset:576
	ds_read_b32 v25, v2 offset:1728
	ds_read_b32 v7, v2 offset:2016
	ds_read_b32 v21, v2 offset:2304
	ds_read_b32 v11, v2 offset:3456
	ds_read_b32 v35, v2 offset:3744
	ds_read_b32 v59, v2 offset:4032
	ds_read_b32 v57, v2 offset:5184
	ds_read_b32 v51, v2 offset:5472
	ds_read_b32 v49, v2 offset:5760
	s_waitcnt lgkmcnt(0)
	v_mov_b32_e32 v64, v32
	v_mov_b32_e32 v46, v43
	v_mov_b32_e32 v65, v61
	v_mov_b64_e32 v[100:101], v[22:23]
	v_mov_b32_dpp v46, v61 row_shr:1 row_mask:0xf bank_mask:0xf
	v_pk_mul_f32 v[86:87], v[64:65], v[46:47]
	v_mov_b32_e32 v26, v19
	v_mov_b32_dpp v43, v60 row_shl:1 row_mask:0xf bank_mask:0xf
	v_pk_fma_f32 v[86:87], v[60:61], v[88:89], v[86:87] op_sel_hi:[0,1,1]
	v_pk_mov_b32 v[60:61], v[60:61], v[100:101] op_sel:[1,0]
	v_mov_b32_dpp v26, v63 row_shr:1 row_mask:0xf bank_mask:0xf
	v_mov_b32_e32 v1, v63
	v_accvgpr_read_b32 v67, a35
	v_pk_fma_f32 v[60:61], v[60:61], v[42:43], v[86:87]
	v_pk_mul_f32 v[86:87], v[0:1], v[26:27]
	v_accvgpr_read_b32 v66, a34
	v_accvgpr_write_b32 a10, v14
	v_mov_b32_dpp v19, v62 row_shl:1 row_mask:0xf bank_mask:0xf
	v_pk_fma_f32 v[86:87], v[62:63], v[16:17], v[86:87] op_sel_hi:[0,1,1]
	v_pk_mov_b32 v[62:63], v[62:63], v[66:67] op_sel:[1,0]
	v_mov_b32_e32 v44, v39
	v_accvgpr_write_b32 a11, v15
	v_pk_fma_f32 v[62:63], v[62:63], v[18:19], v[86:87]
	v_pk_add_f32 v[60:61], v[60:61], 0 op_sel_hi:[1,0]
	v_mov_b32_dpp v44, v69 row_shr:1 row_mask:0xf bank_mask:0xf
	v_mov_b32_e32 v31, v69
	v_accvgpr_read_b32 v14, a16
	v_accvgpr_read_b32 v28, a46
	v_pk_add_f32 v[60:61], v[60:61], v[62:63]
	v_pk_mul_f32 v[62:63], v[30:31], v[44:45]
	v_accvgpr_read_b32 v15, a17
	v_accvgpr_read_b32 v29, a47
	v_mov_b32_dpp v39, v68 row_shl:1 row_mask:0xf bank_mask:0xf
	v_pk_fma_f32 v[62:63], v[68:69], v[14:15], v[62:63] op_sel_hi:[0,1,1]
	v_pk_mov_b32 v[68:69], v[68:69], v[28:29] op_sel:[1,0]
	v_mov_b32_e32 v36, v25
	v_pk_fma_f32 v[62:63], v[68:69], v[38:39], v[62:63]
	s_mov_b64 s[0:1], 0x1400000
	v_pk_add_f32 v[60:61], v[60:61], v[62:63]
	v_mov_b32_dpp v36, v71 row_shr:1 row_mask:0xf bank_mask:0xf
	v_mov_b32_e32 v127, v71
	v_accvgpr_read_b32 v8, a20
	v_lshl_add_u64 v[62:63], v[54:55], 0, s[0:1]
	v_mov_b32_e32 v128, v60
	v_mov_b32_e32 v129, v61
	v_pk_mul_f32 v[60:61], v[126:127], v[36:37]
	v_accvgpr_read_b32 v9, a21
	v_accvgpr_write_b32 a25, v23
	v_mov_b32_e32 v12, v7
	v_mov_b32_dpp v25, v70 row_shl:1 row_mask:0xf bank_mask:0xf
	v_pk_fma_f32 v[60:61], v[70:71], v[8:9], v[60:61] op_sel_hi:[0,1,1]
	v_mov_b32_e32 v62, v71
	v_mov_b32_e32 v63, v101
	v_accvgpr_write_b32 a24, v22
	v_mov_b32_dpp v12, v73 row_shr:1 row_mask:0xf bank_mask:0xf
	v_mov_b32_e32 v74, v52
	v_mov_b32_e32 v75, v73
	v_accvgpr_read_b32 v23, a9
	v_accvgpr_write_b32 a26, v124
	v_accvgpr_mov_b32 a2, a22
	v_pk_fma_f32 v[60:61], v[62:63], v[24:25], v[60:61]
	v_pk_mul_f32 v[62:63], v[74:75], v[12:13]
	v_accvgpr_read_b32 v22, a8
	v_accvgpr_write_b32 a27, v125
	v_accvgpr_mov_b32 a3, a23
	v_accvgpr_write_b32 a22, v88
	v_mov_b32_dpp v7, v72 row_shl:1 row_mask:0xf bank_mask:0xf
	v_pk_fma_f32 v[62:63], v[72:73], v[22:23], v[62:63] op_sel_hi:[0,1,1]
	v_mov_b32_e32 v68, v73
	v_mov_b32_e32 v69, v67
	v_mov_b32_e32 v78, v21
	v_accvgpr_write_b32 a23, v89
	v_pk_fma_f32 v[62:63], v[68:69], v[6:7], v[62:63]
	v_pk_add_f32 v[60:61], v[60:61], 0 op_sel_hi:[1,0]
	v_mov_b32_dpp v78, v83 row_shr:1 row_mask:0xf bank_mask:0xf
	v_accvgpr_read_b32 v52, a30
	v_mov_b32_e32 v53, v83
	v_accvgpr_read_b32 v89, a27
	v_pk_add_f32 v[60:61], v[60:61], v[62:63]
	v_pk_mul_f32 v[62:63], v[52:53], v[78:79]
	v_accvgpr_read_b32 v88, a26
	v_mov_b32_dpp v21, v82 row_shl:1 row_mask:0xf bank_mask:0xf
	v_pk_fma_f32 v[62:63], v[82:83], v[88:89], v[62:63] op_sel_hi:[0,1,1]
	v_mov_b32_e32 v68, v83
	v_mov_b32_e32 v69, v29
	v_pk_fma_f32 v[62:63], v[68:69], v[20:21], v[62:63]
	v_mov_b32_e32 v76, v11
	v_accvgpr_read_b32 v125, a37
	v_pk_add_f32 v[60:61], v[60:61], v[62:63]
	s_mov_b64 s[0:1], 0x1410000
	v_mov_b32_dpp v76, v81 row_shr:1 row_mask:0xf bank_mask:0xf
	v_mov_b32_e32 v121, v81
	v_accvgpr_read_b32 v101, a15
	v_accvgpr_read_b32 v124, a36
	v_lshl_add_u64 v[136:137], v[134:135], 0, s[0:1]
	s_nop 1
	s_mov_b64 vcc, s[28:29]
	s_nop 0
	v_cndmask_b32_dpp v130, v60, v128, vcc quad_perm:[1,0,3,2] row_mask:0xf bank_mask:0xf
	v_cndmask_b32_dpp v131, v61, v129, vcc quad_perm:[1,0,3,2] row_mask:0xf bank_mask:0xf
	s_mov_b64 vcc, s[30:31]
	s_nop 0
	v_cndmask_b32_dpp v132, v128, v60, vcc quad_perm:[1,0,3,2] row_mask:0xf bank_mask:0xf
	v_cndmask_b32_dpp v133, v129, v61, vcc quad_perm:[1,0,3,2] row_mask:0xf bank_mask:0xf
	global_store_dwordx4 v[136:137], v[130:133], off sc0 sc1 nt
	s_nop 1
	v_pk_mul_f32 v[60:61], v[120:121], v[76:77]
	v_accvgpr_read_b32 v100, a14
	v_mov_b32_e32 v2, v35
	v_mov_b32_dpp v11, v80 row_shl:1 row_mask:0xf bank_mask:0xf
	v_pk_fma_f32 v[60:61], v[80:81], v[124:125], v[60:61] op_sel_hi:[0,1,1]
	v_pk_mov_b32 v[62:63], v[80:81], v[100:101] op_sel:[1,0]
	v_mov_b32_dpp v2, v85 row_shr:1 row_mask:0xf bank_mask:0xf
	v_mov_b32_e32 v107, v85
	v_accvgpr_read_b32 v29, a13
	v_pk_fma_f32 v[60:61], v[62:63], v[10:11], v[60:61]
	v_pk_mul_f32 v[62:63], v[106:107], v[2:3]
	v_accvgpr_read_b32 v28, a12
	v_mov_b32_dpp v35, v84 row_shl:1 row_mask:0xf bank_mask:0xf
	v_pk_fma_f32 v[62:63], v[84:85], v[28:29], v[62:63] op_sel_hi:[0,1,1]
	v_pk_mov_b32 v[68:69], v[84:85], v[122:123] op_sel:[1,0]
	v_mov_b32_e32 v92, v59
	v_pk_fma_f32 v[62:63], v[68:69], v[34:35], v[62:63]
	v_pk_add_f32 v[60:61], v[60:61], 0 op_sel_hi:[1,0]
	v_mov_b32_dpp v92, v117 row_shr:1 row_mask:0xf bank_mask:0xf
	v_mov_b32_e32 v97, v117
	v_pk_add_f32 v[60:61], v[60:61], v[62:63]
	v_pk_mul_f32 v[62:63], v[96:97], v[92:93]
	v_accvgpr_write_b32 a8, v118
	v_pk_fma_f32 v[62:63], v[116:117], v[118:119], v[62:63] op_sel_hi:[0,1,1]
	v_accvgpr_write_b32 a9, v119
	v_accvgpr_read_b32 v119, a45
	v_accvgpr_read_b32 v118, a44
	v_mov_b32_dpp v59, v116 row_shl:1 row_mask:0xf bank_mask:0xf
	v_pk_mov_b32 v[68:69], v[116:117], v[118:119] op_sel:[1,0]
	v_mov_b32_e32 v94, v57
	v_pk_fma_f32 v[62:63], v[68:69], v[58:59], v[62:63]
	s_mov_b64 s[0:1], 0x1420000
	v_pk_add_f32 v[60:61], v[60:61], v[62:63]
	v_mov_b32_dpp v94, v115 row_shr:1 row_mask:0xf bank_mask:0xf
	v_mov_b32_e32 v99, v115
	v_accvgpr_read_b32 v41, a11
	v_lshl_add_u64 v[62:63], v[54:55], 0, s[0:1]
	v_mov_b32_e32 v128, v60
	v_mov_b32_e32 v129, v61
	v_pk_mul_f32 v[60:61], v[98:99], v[94:95]
	v_accvgpr_read_b32 v40, a10
	v_mov_b32_e32 v102, v51
	v_mov_b32_dpp v57, v114 row_shl:1 row_mask:0xf bank_mask:0xf
	v_pk_fma_f32 v[60:61], v[114:115], v[40:41], v[60:61] op_sel_hi:[0,1,1]
	v_mov_b32_e32 v62, v115
	v_mov_b32_e32 v63, v101
	v_mov_b32_dpp v102, v113 row_shr:1 row_mask:0xf bank_mask:0xf
	v_mov_b32_e32 v105, v113
	v_pk_fma_f32 v[60:61], v[62:63], v[56:57], v[60:61]
	v_pk_mul_f32 v[62:63], v[104:105], v[102:103]
	v_mov_b32_dpp v51, v112 row_shl:1 row_mask:0xf bank_mask:0xf
	v_pk_fma_f32 v[62:63], v[112:113], v[4:5], v[62:63] op_sel_hi:[0,1,1]
	v_mov_b32_e32 v68, v113
	v_mov_b32_e32 v69, v123
	v_mov_b32_e32 v108, v49
	v_pk_fma_f32 v[62:63], v[68:69], v[50:51], v[62:63]
	v_pk_add_f32 v[60:61], v[60:61], 0 op_sel_hi:[1,0]
	v_mov_b32_dpp v108, v91 row_shr:1 row_mask:0xf bank_mask:0xf
	v_mov_b32_e32 v111, v91
	v_accvgpr_read_b32 v5, a3
	v_pk_add_f32 v[60:61], v[60:61], v[62:63]
	v_pk_mul_f32 v[62:63], v[110:111], v[108:109]
	v_accvgpr_read_b32 v4, a2
	v_mov_b32_dpp v49, v90 row_shl:1 row_mask:0xf bank_mask:0xf
	v_pk_fma_f32 v[62:63], v[90:91], v[4:5], v[62:63] op_sel_hi:[0,1,1]
	v_mov_b32_e32 v68, v91
	v_mov_b32_e32 v69, v119
	v_pk_fma_f32 v[62:63], v[68:69], v[48:49], v[62:63]
	s_mov_b64 s[0:1], 0x1430000
	v_pk_add_f32 v[60:61], v[60:61], v[62:63]
	v_lshl_add_u64 v[136:137], v[134:135], 0, s[0:1]
	s_nop 1
	s_mov_b64 vcc, s[28:29]
	s_nop 0
	v_cndmask_b32_dpp v130, v60, v128, vcc quad_perm:[1,0,3,2] row_mask:0xf bank_mask:0xf
	v_cndmask_b32_dpp v131, v61, v129, vcc quad_perm:[1,0,3,2] row_mask:0xf bank_mask:0xf
	s_mov_b64 vcc, s[30:31]
	s_nop 0
	v_cndmask_b32_dpp v132, v128, v60, vcc quad_perm:[1,0,3,2] row_mask:0xf bank_mask:0xf
	v_cndmask_b32_dpp v133, v129, v61, vcc quad_perm:[1,0,3,2] row_mask:0xf bank_mask:0xf
	global_store_dwordx4 v[136:137], v[130:133], off sc0 sc1 nt
	s_nop 1
	s_waitcnt vmcnt(12)
	s_waitcnt lgkmcnt(0)
	s_barrier
	v_accvgpr_read_b32 v2, a1
	v_accvgpr_read_b32 v12, a5
	ds_read_b64 v[60:61], v12
	ds_read_b64 v[62:63], v12 offset:288
	ds_read_b64 v[68:69], v12 offset:576
	ds_read_b64 v[70:71], v12 offset:1728
	ds_read_b64 v[72:73], v12 offset:2016
	ds_read_b64 v[82:83], v12 offset:2304
	ds_read_b64 v[80:81], v12 offset:3456
	ds_read_b64 v[84:85], v12 offset:3744
	ds_read_b64 v[116:117], v12 offset:4032
	ds_read_b64 v[114:115], v12 offset:5184
	ds_read_b64 v[112:113], v12 offset:5472
	ds_read_b64 v[90:91], v12 offset:5760
	ds_read_b32 v43, v2
	ds_read_b32 v19, v2 offset:288
	ds_read_b32 v39, v2 offset:576
	ds_read_b32 v25, v2 offset:1728
	ds_read_b32 v7, v2 offset:2016
	ds_read_b32 v21, v2 offset:2304
	ds_read_b32 v11, v2 offset:3456
	ds_read_b32 v35, v2 offset:3744
	ds_read_b32 v59, v2 offset:4032
	ds_read_b32 v57, v2 offset:5184
	ds_read_b32 v51, v2 offset:5472
	ds_read_b32 v49, v2 offset:5760
	s_waitcnt lgkmcnt(0)
	v_accvgpr_read_b32 v101, a23
	v_mov_b32_e32 v46, v43
	v_mov_b32_e32 v65, v61
	v_accvgpr_read_b32 v31, a25
	v_mov_b32_dpp v46, v61 row_shr:1 row_mask:0xf bank_mask:0xf
	v_pk_mul_f32 v[86:87], v[64:65], v[46:47]
	v_accvgpr_read_b32 v100, a22
	v_accvgpr_read_b32 v30, a24
	v_mov_b32_e32 v26, v19
	v_mov_b32_dpp v43, v60 row_shl:1 row_mask:0xf bank_mask:0xf
	v_pk_fma_f32 v[86:87], v[60:61], v[100:101], v[86:87] op_sel_hi:[0,1,1]
	v_pk_mov_b32 v[60:61], v[60:61], v[30:31] op_sel:[1,0]
	v_mov_b32_dpp v26, v63 row_shr:1 row_mask:0xf bank_mask:0xf
	v_mov_b32_e32 v1, v63
	v_pk_fma_f32 v[60:61], v[60:61], v[42:43], v[86:87]
	v_pk_mul_f32 v[86:87], v[0:1], v[26:27]
	v_accvgpr_read_b32 v0, a34
	v_accvgpr_mov_b32 a12, a14
	v_accvgpr_read_b32 v1, a35
	v_accvgpr_mov_b32 a13, a15
	v_mov_b32_dpp v19, v62 row_shl:1 row_mask:0xf bank_mask:0xf
	v_pk_fma_f32 v[86:87], v[62:63], v[16:17], v[86:87] op_sel_hi:[0,1,1]
	v_accvgpr_write_b32 a14, v16
	v_pk_mov_b32 v[62:63], v[62:63], v[0:1] op_sel:[1,0]
	v_mov_b32_e32 v44, v39
	v_accvgpr_write_b32 a15, v17
	v_pk_fma_f32 v[62:63], v[62:63], v[18:19], v[86:87]
	v_pk_add_f32 v[60:61], v[60:61], 0 op_sel_hi:[1,0]
	v_mov_b32_dpp v44, v69 row_shr:1 row_mask:0xf bank_mask:0xf
	v_accvgpr_read_b32 v16, a48
	v_mov_b32_e32 v17, v69
	v_accvgpr_read_b32 v67, a47
	v_pk_add_f32 v[60:61], v[60:61], v[62:63]
	v_pk_mul_f32 v[62:63], v[16:17], v[44:45]
	v_accvgpr_read_b32 v66, a46
	v_mov_b32_dpp v39, v68 row_shl:1 row_mask:0xf bank_mask:0xf
	v_pk_fma_f32 v[62:63], v[68:69], v[14:15], v[62:63] op_sel_hi:[0,1,1]
	v_pk_mov_b32 v[68:69], v[68:69], v[66:67] op_sel:[1,0]
	v_mov_b32_e32 v36, v25
	v_pk_fma_f32 v[62:63], v[68:69], v[38:39], v[62:63]
	s_mov_b64 s[0:1], 0x1800000
	v_pk_add_f32 v[60:61], v[60:61], v[62:63]
	v_mov_b32_dpp v36, v71 row_shr:1 row_mask:0xf bank_mask:0xf
	v_mov_b32_e32 v127, v71
	v_lshl_add_u64 v[62:63], v[54:55], 0, s[0:1]
	v_mov_b32_e32 v128, v60
	v_mov_b32_e32 v129, v61
	v_pk_mul_f32 v[60:61], v[126:127], v[36:37]
	v_mov_b32_e32 v12, v7
	v_mov_b32_dpp v25, v70 row_shl:1 row_mask:0xf bank_mask:0xf
	v_pk_fma_f32 v[60:61], v[70:71], v[8:9], v[60:61] op_sel_hi:[0,1,1]
	v_mov_b32_e32 v62, v71
	v_mov_b32_e32 v63, v31
	v_mov_b32_dpp v12, v73 row_shr:1 row_mask:0xf bank_mask:0xf
	v_mov_b32_e32 v75, v73
	v_pk_fma_f32 v[60:61], v[62:63], v[24:25], v[60:61]
	v_pk_mul_f32 v[62:63], v[74:75], v[12:13]
	v_mov_b32_dpp v7, v72 row_shl:1 row_mask:0xf bank_mask:0xf
	v_pk_fma_f32 v[62:63], v[72:73], v[22:23], v[62:63] op_sel_hi:[0,1,1]
	v_accvgpr_write_b32 a4, v22
	v_mov_b32_e32 v68, v73
	v_mov_b32_e32 v69, v1
	v_mov_b32_e32 v78, v21
	v_accvgpr_write_b32 a5, v23
	v_pk_fma_f32 v[62:63], v[68:69], v[6:7], v[62:63]
	v_pk_add_f32 v[60:61], v[60:61], 0 op_sel_hi:[1,0]
	v_mov_b32_dpp v78, v83 row_shr:1 row_mask:0xf bank_mask:0xf
	v_mov_b32_e32 v53, v83
	v_accvgpr_read_b32 v22, a26
	v_pk_add_f32 v[60:61], v[60:61], v[62:63]
	v_pk_mul_f32 v[62:63], v[52:53], v[78:79]
	v_accvgpr_read_b32 v23, a27
	v_mov_b32_dpp v21, v82 row_shl:1 row_mask:0xf bank_mask:0xf
	v_pk_fma_f32 v[62:63], v[82:83], v[22:23], v[62:63] op_sel_hi:[0,1,1]
	v_mov_b32_e32 v68, v83
	v_mov_b32_e32 v69, v67
	v_pk_fma_f32 v[62:63], v[68:69], v[20:21], v[62:63]
	v_mov_b32_e32 v76, v11
	v_pk_add_f32 v[60:61], v[60:61], v[62:63]
	s_mov_b64 s[0:1], 0x1810000
	v_mov_b32_dpp v76, v81 row_shr:1 row_mask:0xf bank_mask:0xf
	v_mov_b32_e32 v121, v81
	v_accvgpr_read_b32 v15, a13
	v_lshl_add_u64 v[136:137], v[134:135], 0, s[0:1]
	s_nop 1
	s_mov_b64 vcc, s[28:29]
	s_nop 0
	v_cndmask_b32_dpp v130, v60, v128, vcc quad_perm:[1,0,3,2] row_mask:0xf bank_mask:0xf
	v_cndmask_b32_dpp v131, v61, v129, vcc quad_perm:[1,0,3,2] row_mask:0xf bank_mask:0xf
	s_mov_b64 vcc, s[30:31]
	s_nop 0
	v_cndmask_b32_dpp v132, v128, v60, vcc quad_perm:[1,0,3,2] row_mask:0xf bank_mask:0xf
	v_cndmask_b32_dpp v133, v129, v61, vcc quad_perm:[1,0,3,2] row_mask:0xf bank_mask:0xf
	global_store_dwordx4 v[136:137], v[130:133], off sc0 sc1 nt
	s_nop 1
	v_pk_mul_f32 v[60:61], v[120:121], v[76:77]
	v_accvgpr_read_b32 v14, a12
	v_mov_b32_e32 v2, v35
	v_mov_b32_dpp v11, v80 row_shl:1 row_mask:0xf bank_mask:0xf
	v_pk_fma_f32 v[60:61], v[80:81], v[124:125], v[60:61] op_sel_hi:[0,1,1]
	v_pk_mov_b32 v[62:63], v[80:81], v[14:15] op_sel:[1,0]
	v_mov_b32_dpp v2, v85 row_shr:1 row_mask:0xf bank_mask:0xf
	v_mov_b32_e32 v107, v85
	v_pk_fma_f32 v[60:61], v[62:63], v[10:11], v[60:61]
	v_pk_mul_f32 v[62:63], v[106:107], v[2:3]
	v_mov_b32_dpp v35, v84 row_shl:1 row_mask:0xf bank_mask:0xf
	v_pk_fma_f32 v[62:63], v[84:85], v[28:29], v[62:63] op_sel_hi:[0,1,1]
	v_pk_mov_b32 v[68:69], v[84:85], v[122:123] op_sel:[1,0]
	v_mov_b32_e32 v92, v59
	v_pk_fma_f32 v[62:63], v[68:69], v[34:35], v[62:63]
	v_pk_add_f32 v[60:61], v[60:61], 0 op_sel_hi:[1,0]
	v_mov_b32_dpp v92, v117 row_shr:1 row_mask:0xf bank_mask:0xf
	v_mov_b32_e32 v97, v117
	v_accvgpr_read_b32 v87, a9
	v_pk_add_f32 v[60:61], v[60:61], v[62:63]
	v_pk_mul_f32 v[62:63], v[96:97], v[92:93]
	v_accvgpr_read_b32 v86, a8
	v_mov_b32_dpp v59, v116 row_shl:1 row_mask:0xf bank_mask:0xf
	v_pk_fma_f32 v[62:63], v[116:117], v[86:87], v[62:63] op_sel_hi:[0,1,1]
	v_pk_mov_b32 v[68:69], v[116:117], v[118:119] op_sel:[1,0]
	v_mov_b32_e32 v94, v57
	v_pk_fma_f32 v[62:63], v[68:69], v[58:59], v[62:63]
	s_mov_b64 s[0:1], 0x1820000
	v_pk_add_f32 v[60:61], v[60:61], v[62:63]
	v_mov_b32_dpp v94, v115 row_shr:1 row_mask:0xf bank_mask:0xf
	v_mov_b32_e32 v99, v115
	v_lshl_add_u64 v[62:63], v[54:55], 0, s[0:1]
	v_mov_b32_e32 v128, v60
	v_mov_b32_e32 v129, v61
	v_pk_mul_f32 v[60:61], v[98:99], v[94:95]
	v_mov_b32_e32 v102, v51
	v_mov_b32_dpp v57, v114 row_shl:1 row_mask:0xf bank_mask:0xf
	v_pk_fma_f32 v[60:61], v[114:115], v[40:41], v[60:61] op_sel_hi:[0,1,1]
	v_mov_b32_e32 v62, v115
	v_mov_b32_e32 v63, v15
	v_mov_b32_dpp v102, v113 row_shr:1 row_mask:0xf bank_mask:0xf
	v_mov_b32_e32 v105, v113
	v_accvgpr_read_b32 v89, a19
	v_pk_fma_f32 v[60:61], v[62:63], v[56:57], v[60:61]
	v_pk_mul_f32 v[62:63], v[104:105], v[102:103]
	v_accvgpr_read_b32 v88, a18
	v_mov_b32_dpp v51, v112 row_shl:1 row_mask:0xf bank_mask:0xf
	v_pk_fma_f32 v[62:63], v[112:113], v[88:89], v[62:63] op_sel_hi:[0,1,1]
	v_mov_b32_e32 v68, v113
	v_mov_b32_e32 v69, v123
	v_mov_b32_e32 v108, v49
	v_pk_fma_f32 v[62:63], v[68:69], v[50:51], v[62:63]
	v_pk_add_f32 v[60:61], v[60:61], 0 op_sel_hi:[1,0]
	v_mov_b32_dpp v108, v91 row_shr:1 row_mask:0xf bank_mask:0xf
	v_mov_b32_e32 v111, v91
	v_pk_add_f32 v[60:61], v[60:61], v[62:63]
	v_pk_mul_f32 v[62:63], v[110:111], v[108:109]
	v_mov_b32_dpp v49, v90 row_shl:1 row_mask:0xf bank_mask:0xf
	v_pk_fma_f32 v[62:63], v[90:91], v[4:5], v[62:63] op_sel_hi:[0,1,1]
	v_mov_b32_e32 v68, v91
	v_mov_b32_e32 v69, v119
	v_pk_fma_f32 v[62:63], v[68:69], v[48:49], v[62:63]
	s_mov_b64 s[0:1], 0x1830000
	v_pk_add_f32 v[60:61], v[60:61], v[62:63]
	v_lshl_add_u64 v[136:137], v[134:135], 0, s[0:1]
	s_nop 1
	s_mov_b64 vcc, s[28:29]
	s_nop 0
	v_cndmask_b32_dpp v130, v60, v128, vcc quad_perm:[1,0,3,2] row_mask:0xf bank_mask:0xf
	v_cndmask_b32_dpp v131, v61, v129, vcc quad_perm:[1,0,3,2] row_mask:0xf bank_mask:0xf
	s_mov_b64 vcc, s[30:31]
	s_nop 0
	v_cndmask_b32_dpp v132, v128, v60, vcc quad_perm:[1,0,3,2] row_mask:0xf bank_mask:0xf
	v_cndmask_b32_dpp v133, v129, v61, vcc quad_perm:[1,0,3,2] row_mask:0xf bank_mask:0xf
	global_store_dwordx4 v[136:137], v[130:133], off sc0 sc1 nt
	s_nop 1
	v_accvgpr_write_b32 a12, v28
	s_waitcnt vmcnt(8)
	v_accvgpr_write_b32 a13, v29
	v_mov_b64_e32 v[28:29], v[4:5]
	s_waitcnt lgkmcnt(0)
	s_barrier
	v_accvgpr_read_b32 v2, a6
	v_accvgpr_read_b32 v4, a7
	ds_read_b64 v[60:61], v2
	ds_read_b64 v[62:63], v2 offset:288
	ds_read_b64 v[68:69], v2 offset:576
	ds_read_b64 v[70:71], v2 offset:1728
	ds_read_b64 v[72:73], v2 offset:2016
	ds_read_b64 v[82:83], v2 offset:2304
	ds_read_b64 v[80:81], v2 offset:3456
	ds_read_b64 v[84:85], v2 offset:3744
	ds_read_b64 v[116:117], v2 offset:4032
	ds_read_b64 v[114:115], v2 offset:5184
	ds_read_b64 v[112:113], v2 offset:5472
	ds_read_b64 v[90:91], v2 offset:5760
	ds_read_b32 v43, v4
	ds_read_b32 v19, v4 offset:288
	ds_read_b32 v39, v4 offset:576
	ds_read_b32 v25, v4 offset:1728
	ds_read_b32 v7, v4 offset:2016
	ds_read_b32 v21, v4 offset:2304
	ds_read_b32 v11, v4 offset:3456
	ds_read_b32 v35, v4 offset:3744
	ds_read_b32 v59, v4 offset:4032
	ds_read_b32 v57, v4 offset:5184
	ds_read_b32 v51, v4 offset:5472
	ds_read_b32 v49, v4 offset:5760
	s_waitcnt lgkmcnt(0)
	v_accvgpr_read_b32 v8, a24
	v_mov_b32_e32 v46, v43
	v_mov_b32_e32 v65, v61
	v_mov_b32_e32 v26, v19
	v_mov_b32_dpp v46, v61 row_shr:1 row_mask:0xf bank_mask:0xf
	v_accvgpr_read_b32 v32, a32
	v_accvgpr_read_b32 v9, a25
	v_mov_b64_e32 v[124:125], v[40:41]
	v_pk_mul_f32 v[30:31], v[64:65], v[46:47]
	v_mov_b32_dpp v26, v63 row_shr:1 row_mask:0xf bank_mask:0xf
	v_mov_b32_e32 v33, v63
	v_accvgpr_read_b32 v4, a14
	v_accvgpr_read_b32 v41, a35
	v_mov_b32_e32 v44, v39
	v_pk_fma_f32 v[30:31], v[60:61], v[100:101], v[30:31] op_sel_hi:[0,1,1]
	v_mov_b32_dpp v43, v60 row_shl:1 row_mask:0xf bank_mask:0xf
	v_pk_mov_b32 v[46:47], v[60:61], v[8:9] op_sel:[1,0]
	v_pk_mul_f32 v[26:27], v[32:33], v[26:27]
	v_accvgpr_read_b32 v5, a15
	v_accvgpr_read_b32 v40, a34
	v_mov_b32_dpp v44, v69 row_shr:1 row_mask:0xf bank_mask:0xf
	v_mov_b32_e32 v17, v69
	v_accvgpr_read_b32 v0, a16
	v_pk_fma_f32 v[30:31], v[46:47], v[42:43], v[30:31]
	v_pk_fma_f32 v[26:27], v[62:63], v[4:5], v[26:27] op_sel_hi:[0,1,1]
	v_mov_b32_dpp v19, v62 row_shl:1 row_mask:0xf bank_mask:0xf
	v_pk_mov_b32 v[32:33], v[62:63], v[40:41] op_sel:[1,0]
	v_pk_mul_f32 v[16:17], v[16:17], v[44:45]
	v_accvgpr_read_b32 v1, a17
	v_pk_fma_f32 v[18:19], v[32:33], v[18:19], v[26:27]
	v_pk_add_f32 v[26:27], v[30:31], 0 op_sel_hi:[1,0]
	v_mov_b32_dpp v39, v68 row_shl:1 row_mask:0xf bank_mask:0xf
	v_pk_fma_f32 v[16:17], v[68:69], v[0:1], v[16:17] op_sel_hi:[0,1,1]
	v_pk_mov_b32 v[30:31], v[68:69], v[66:67] op_sel:[1,0]
	v_pk_add_f32 v[18:19], v[26:27], v[18:19]
	v_pk_fma_f32 v[16:17], v[30:31], v[38:39], v[16:17]
	v_mov_b32_e32 v36, v25
	s_mov_b64 s[0:1], 0x1c00000
	v_pk_add_f32 v[16:17], v[18:19], v[16:17]
	v_mov_b32_dpp v36, v71 row_shr:1 row_mask:0xf bank_mask:0xf
	v_mov_b32_e32 v127, v71
	v_accvgpr_read_b32 v0, a20
	v_lshl_add_u64 v[26:27], v[54:55], 0, s[0:1]
	v_mov_b32_e32 v128, v16
	v_mov_b32_e32 v129, v17
	v_mov_b32_e32 v12, v7
	v_pk_mul_f32 v[16:17], v[126:127], v[36:37]
	v_accvgpr_read_b32 v1, a21
	v_mov_b32_dpp v12, v73 row_shr:1 row_mask:0xf bank_mask:0xf
	v_pk_fma_f32 v[16:17], v[70:71], v[0:1], v[16:17] op_sel_hi:[0,1,1]
	v_mov_b32_e32 v75, v73
	v_accvgpr_read_b32 v0, a4
	v_mov_b32_e32 v78, v21
	v_pk_mul_f32 v[12:13], v[74:75], v[12:13]
	v_accvgpr_read_b32 v1, a5
	v_mov_b32_dpp v25, v70 row_shl:1 row_mask:0xf bank_mask:0xf
	v_mov_b32_dpp v7, v72 row_shl:1 row_mask:0xf bank_mask:0xf
	v_mov_b32_dpp v78, v83 row_shr:1 row_mask:0xf bank_mask:0xf
	v_mov_b32_e32 v8, v71
	v_pk_fma_f32 v[12:13], v[72:73], v[0:1], v[12:13] op_sel_hi:[0,1,1]
	v_mov_b32_e32 v5, v41
	v_mov_b32_e32 v4, v73
	v_mov_b32_e32 v53, v83
	v_pk_fma_f32 v[16:17], v[8:9], v[24:25], v[16:17]
	v_pk_fma_f32 v[6:7], v[4:5], v[6:7], v[12:13]
	v_pk_mul_f32 v[12:13], v[52:53], v[78:79]
	v_mov_b32_dpp v21, v82 row_shl:1 row_mask:0xf bank_mask:0xf
	v_pk_add_f32 v[16:17], v[16:17], 0 op_sel_hi:[1,0]
	v_pk_fma_f32 v[12:13], v[82:83], v[22:23], v[12:13] op_sel_hi:[0,1,1]
	v_mov_b32_e32 v66, v83
	v_pk_add_f32 v[6:7], v[16:17], v[6:7]
	v_pk_fma_f32 v[12:13], v[66:67], v[20:21], v[12:13]
	v_mov_b32_e32 v76, v11
	v_pk_add_f32 v[6:7], v[6:7], v[12:13]
	s_mov_b64 s[0:1], 0x1c10000
	v_mov_b32_dpp v76, v81 row_shr:1 row_mask:0xf bank_mask:0xf
	v_mov_b32_e32 v121, v81
	v_accvgpr_read_b32 v0, a36
	v_lshl_add_u64 v[136:137], v[134:135], 0, s[0:1]
	s_nop 1
	s_mov_b64 vcc, s[28:29]
	s_nop 0
	v_cndmask_b32_dpp v130, v6, v128, vcc quad_perm:[1,0,3,2] row_mask:0xf bank_mask:0xf
	v_cndmask_b32_dpp v131, v7, v129, vcc quad_perm:[1,0,3,2] row_mask:0xf bank_mask:0xf
	s_mov_b64 vcc, s[30:31]
	s_nop 0
	v_cndmask_b32_dpp v132, v128, v6, vcc quad_perm:[1,0,3,2] row_mask:0xf bank_mask:0xf
	v_cndmask_b32_dpp v133, v129, v7, vcc quad_perm:[1,0,3,2] row_mask:0xf bank_mask:0xf
	global_store_dwordx4 v[136:137], v[130:133], off sc0 sc1 nt
	s_nop 1
	v_mov_b32_e32 v2, v35
	v_pk_mul_f32 v[6:7], v[120:121], v[76:77]
	v_accvgpr_read_b32 v1, a37
	v_mov_b32_dpp v2, v85 row_shr:1 row_mask:0xf bank_mask:0xf
	v_pk_fma_f32 v[6:7], v[80:81], v[0:1], v[6:7] op_sel_hi:[0,1,1]
	v_mov_b32_e32 v107, v85
	v_accvgpr_read_b32 v0, a12
	v_mov_b32_e32 v92, v59
	v_pk_mul_f32 v[2:3], v[106:107], v[2:3]
	v_accvgpr_read_b32 v1, a13
	v_mov_b32_dpp v11, v80 row_shl:1 row_mask:0xf bank_mask:0xf
	v_mov_b32_dpp v35, v84 row_shl:1 row_mask:0xf bank_mask:0xf
	v_mov_b32_dpp v92, v117 row_shr:1 row_mask:0xf bank_mask:0xf
	v_pk_mov_b32 v[8:9], v[80:81], v[14:15] op_sel:[1,0]
	v_pk_fma_f32 v[2:3], v[84:85], v[0:1], v[2:3] op_sel_hi:[0,1,1]
	v_pk_mov_b32 v[4:5], v[84:85], v[122:123] op_sel:[1,0]
	v_mov_b32_e32 v97, v117
	v_pk_fma_f32 v[6:7], v[8:9], v[10:11], v[6:7]
	v_pk_fma_f32 v[0:1], v[4:5], v[34:35], v[2:3]
	v_pk_mul_f32 v[2:3], v[96:97], v[92:93]
	v_mov_b32_dpp v59, v116 row_shl:1 row_mask:0xf bank_mask:0xf
	v_pk_add_f32 v[6:7], v[6:7], 0 op_sel_hi:[1,0]
	v_pk_fma_f32 v[2:3], v[116:117], v[86:87], v[2:3] op_sel_hi:[0,1,1]
	v_pk_mov_b32 v[4:5], v[116:117], v[118:119] op_sel:[1,0]
	v_pk_add_f32 v[0:1], v[6:7], v[0:1]
	v_pk_fma_f32 v[2:3], v[4:5], v[58:59], v[2:3]
	v_mov_b32_e32 v94, v57
	v_pk_add_f32 v[0:1], v[0:1], v[2:3]
	s_mov_b64 s[0:1], 0x1c20000
	v_mov_b32_dpp v94, v115 row_shr:1 row_mask:0xf bank_mask:0xf
	v_mov_b32_e32 v102, v51
	v_mov_b32_e32 v99, v115
	v_lshl_add_u64 v[2:3], v[54:55], 0, s[0:1]
	v_mov_b32_e32 v128, v0
	v_mov_b32_e32 v129, v1
	v_mov_b32_dpp v102, v113 row_shr:1 row_mask:0xf bank_mask:0xf
	v_pk_mul_f32 v[0:1], v[98:99], v[94:95]
	v_mov_b32_e32 v105, v113
	v_mov_b32_dpp v57, v114 row_shl:1 row_mask:0xf bank_mask:0xf
	v_pk_fma_f32 v[0:1], v[114:115], v[124:125], v[0:1] op_sel_hi:[0,1,1]
	v_mov_b32_e32 v14, v115
	v_pk_mul_f32 v[2:3], v[104:105], v[102:103]
	v_mov_b32_dpp v51, v112 row_shl:1 row_mask:0xf bank_mask:0xf
	v_mov_b32_e32 v108, v49
	v_pk_fma_f32 v[0:1], v[14:15], v[56:57], v[0:1]
	v_pk_fma_f32 v[2:3], v[112:113], v[88:89], v[2:3] op_sel_hi:[0,1,1]
	v_mov_b32_e32 v122, v113
	v_mov_b32_dpp v108, v91 row_shr:1 row_mask:0xf bank_mask:0xf
	v_pk_add_f32 v[0:1], v[0:1], 0 op_sel_hi:[1,0]
	v_pk_fma_f32 v[2:3], v[122:123], v[50:51], v[2:3]
	v_mov_b32_e32 v111, v91
	v_pk_add_f32 v[0:1], v[0:1], v[2:3]
	v_pk_mul_f32 v[2:3], v[110:111], v[108:109]
	v_mov_b32_dpp v49, v90 row_shl:1 row_mask:0xf bank_mask:0xf
	v_pk_fma_f32 v[2:3], v[90:91], v[28:29], v[2:3] op_sel_hi:[0,1,1]
	v_mov_b32_e32 v118, v91
	v_pk_fma_f32 v[2:3], v[118:119], v[48:49], v[2:3]
	s_mov_b64 s[0:1], 0x1c30000
	v_pk_add_f32 v[0:1], v[0:1], v[2:3]
	v_lshl_add_u64 v[136:137], v[134:135], 0, s[0:1]
	s_nop 1
	s_mov_b64 vcc, s[28:29]
	s_nop 0
	v_cndmask_b32_dpp v130, v0, v128, vcc quad_perm:[1,0,3,2] row_mask:0xf bank_mask:0xf
	v_cndmask_b32_dpp v131, v1, v129, vcc quad_perm:[1,0,3,2] row_mask:0xf bank_mask:0xf
	s_mov_b64 vcc, s[30:31]
	s_nop 0
	v_cndmask_b32_dpp v132, v128, v0, vcc quad_perm:[1,0,3,2] row_mask:0xf bank_mask:0xf
	v_cndmask_b32_dpp v133, v129, v1, vcc quad_perm:[1,0,3,2] row_mask:0xf bank_mask:0xf
	global_store_dwordx4 v[136:137], v[130:133], off sc0 sc1 nt
	s_nop 1
	s_endpgm
